# xnorm: the loop-invariant gate parameters (dt_bias, a_log, b_fgate of the lane's logit column) loaded once in front of the loop instead of inside divergent branches for every row (8 exposed round trip
# speedup vs baseline: 1.0236x; 1.0067x over previous
; DI float sigmoidf_(float x) { return __builtin_amdgcn_rcpf(1.f + __expf(-x)); }
; DI float softplusf_(float x) { return fmaxf(x, 0.f) + log1pf(__expf(-fabsf(x))); }
; DI void phase_xnorm(const Params& p, int bid, int nb, char* lds) {
;     ...
;   for (int row0 = gw * 4; row0 < T_; row0 += nw * 4) {
;     ...
;     if (fq == 0) {
;       const int j = fr;
; #pragma unroll
;       for (int r = 0; r < 4; ++r) { const float xx = acc[r]; float res;
;         if (j < 8) res = -softplusf_(-(xx + p.b_fgate[j]));
;         else if (j < 12) res = sigmoidf_(xx);
;         else res = -__expf(p.a_log[j - 12]) * softplusf_(xx + p.dt_bias[j - 12]);
.LBB0_90:
	s_or_b64 exec, exec, s[0:1]
	v_ashrrev_i32_e32 v0, 6, v2
	v_lshlrev_b32_e32 v188, 4, v176
	s_add_u32 s20, s84, 0x100000
	v_lshl_add_u32 v88, v0, 2, v188
	s_mov_b32 s0, 0x8000
	s_addc_u32 s21, s85, 0
	v_cmp_gt_i32_e32 vcc, s0, v88
	v_mbcnt_lo_u32_b32 v177, -1, 0
	s_waitcnt lgkmcnt(0)
	s_barrier
	s_and_saveexec_b64 s[0:1], vcc
	s_cbranch_execz .LBB0_127
	v_mbcnt_hi_u32_b32 v4, -1, v177
	v_and_b32_e32 v5, 64, v4
	v_add_u32_e32 v5, 64, v5
	v_xor_b32_e32 v6, 32, v4
	s_movk_i32 s2, 0x2040
	v_cmp_lt_i32_e32 vcc, v6, v5
	v_mad_u64_u32 v[90:91], s[2:3], v0, s2, v[146:147]
	s_nop 0
	v_cndmask_b32_e32 v6, v4, v6, vcc
	v_lshlrev_b32_e32 v91, 2, v6
	v_xor_b32_e32 v6, 16, v4
	v_cmp_lt_i32_e32 vcc, v6, v5
	v_and_b32_e32 v3, 15, v2
	v_mov_b32_e32 v93, 0
	v_cndmask_b32_e32 v6, v4, v6, vcc
	v_lshlrev_b32_e32 v136, 2, v6
	v_xor_b32_e32 v6, 8, v4
	v_cmp_lt_i32_e32 vcc, v6, v5
	v_and_b32_e32 v1, 63, v2
	v_ashrrev_i32_e32 v89, 31, v88
	v_cndmask_b32_e32 v6, v4, v6, vcc
	v_lshlrev_b32_e32 v137, 2, v6
	v_xor_b32_e32 v6, 4, v4
	v_cmp_lt_i32_e32 vcc, v6, v5
	v_lshlrev_b32_e32 v0, 2, v1
	s_movk_i32 s2, 0x810
	v_cndmask_b32_e32 v6, v4, v6, vcc
	v_lshlrev_b32_e32 v138, 2, v6
	v_xor_b32_e32 v6, 2, v4
	v_cmp_lt_i32_e32 vcc, v6, v5
	v_lshlrev_b32_e32 v8, 4, v1
	v_and_b32_e32 v7, 48, v2
	v_cndmask_b32_e32 v6, v4, v6, vcc
	v_lshlrev_b32_e32 v139, 2, v6
	v_xor_b32_e32 v6, 1, v4
	v_cmp_lt_i32_e32 vcc, v6, v5
	s_lshl_b32 s10, s86, 5
	v_mov_b32_e32 v9, v93
	v_cndmask_b32_e32 v4, v4, v6, vcc
	v_subrev_co_u32_e32 v92, vcc, 12, v3
	v_lshlrev_b64 v[10:11], 2, v[92:93]
	v_lshlrev_b32_e32 v140, 2, v4
	v_and_b32_e32 v4, 3, v2
	v_lshl_add_u64 v[96:97], s[72:73], 0, v[10:11]
	v_lshl_add_u64 v[98:99], s[74:75], 0, v[10:11]
	v_lshlrev_b64 v[10:11], 12, v[88:89]
	v_mad_u32_u24 v5, v4, s2, v90
	v_or_b32_e32 v2, 0x100, v0
	v_or_b32_e32 v4, 0x200, v0
	v_or_b32_e32 v6, 0x300, v0
	v_or_b32_e32 v10, v10, v8
	v_mad_u32_u24 v12, v3, s2, v146
	v_lshlrev_b32_e32 v141, 3, v1
	v_lshlrev_b32_e32 v13, 1, v2
	v_lshlrev_b32_e32 v14, 1, v4
	v_lshlrev_b32_e32 v15, 1, v6
	v_lshl_add_u64 v[94:95], s[44:45], 0, v[8:9]
	v_lshlrev_b32_e32 v92, 2, v3
	v_lshlrev_b64 v[102:103], 6, v[88:89]
	s_ashr_i32 s11, s10, 31
	v_lshlrev_b64 v[104:105], 11, v[88:89]
	v_lshl_add_u64 v[8:9], s[36:37], 0, v[10:11]
	s_mov_b64 s[2:3], 0x3c00
	v_cmp_gt_u32_e64 s[4:5], 16, v1
	v_cmp_lt_u32_e64 s[6:7], 7, v3
	s_xor_b64 s[8:9], vcc, -1
	v_lshl_add_u64 v[100:101], s[50:51], 0, v[92:93]
	v_and_b32_e32 v243, 15, v206
	v_subrev_u32_e32 v244, 12, v243
	v_max_i32_e32 v244, 0, v244
	v_lshlrev_b32_e32 v244, 2, v244
	v_min_u32_e32 v243, 7, v243
	v_lshlrev_b32_e32 v243, 2, v243
	global_load_dword v240, v244, s[74:75]
	global_load_dword v241, v244, s[72:73]
	global_load_dword v242, v243, s[50:51]
	v_or_b32_e32 v102, v102, v92
	s_lshl_b64 s[12:13], s[10:11], 6
	v_or_b32_e32 v104, v104, v141
	s_lshl_b64 s[14:15], s[10:11], 11
	v_lshl_add_u64 v[106:107], v[8:9], 0, s[2:3]
	s_lshl_b64 s[16:17], s[10:11], 12
	s_mov_b64 s[22:23], 0
	s_mov_b64 s[24:25], 0x1000
	v_lshlrev_b32_e32 v92, 2, v0
	v_lshlrev_b32_e32 v108, 2, v2
	v_lshlrev_b32_e32 v110, 2, v4
	v_lshlrev_b32_e32 v112, 2, v6
	s_mov_b32 s26, 0x3a800000
	s_mov_b32 s28, 0x358637bd
	s_mov_b32 s2, 0x800000
	s_brev_b32 s3, 64
	v_add_u32_e32 v89, v90, v13
	v_add_u32_e32 v142, v90, v14
	v_add_u32_e32 v143, v90, v15
	s_mov_b32 s11, 0x2001000
	v_add_u32_e32 v144, v5, v7
	v_add_u32_e32 v145, v12, v7
	s_mov_b32 s18, 0xbfb8aa3b
	s_mov_b32 s19, 0x3f2aaaab
	v_mov_b32_e32 v148, 0x3ecc95a3
	s_mov_b32 s27, 0x3f317218
	s_mov_b32 s29, 0x7f800000
	s_mov_b32 s40, 0x33800000
	s_movk_i32 s41, 0x7fff
	v_mov_b32_e32 v114, 0x3f317218
	v_mov_b32_e32 v149, 0x7f800000
	v_mov_b32_e32 v150, 0x7fc00000
	v_mov_b32_e32 v151, 0xff800000
	s_branch .LBB0_94

; DI void phase_xnorm(const Params& p, int bid, int nb, char* lds) {
;     ...
;   for (int row0 = gw * 4; row0 < T_; row0 += nw * 4) {
;     const int b = row0 >> 13;
;     f32x4 v[4][4];
; #pragma unroll
;     for (int r = 0; r < 4; ++r)
; #pragma unroll
;       for (int i = 0; i < 4; ++i) v[r][i] = ((const f32x4*)(p.x + (size_t)(row0 + r) * 1024))[lane + 64 * i];
;     f32x4 g4[4], sh[4], sc[4];
; #pragma unroll
;     for (int i = 0; i < 4; ++i) { const int col = 4 * lane + 256 * i; g4[i] = *(const f32x4*)(p.g_pre_mix + col); sh[i] = *(const f32x4*)(mod + b * 6144 + col); sc[i] = *(const f32x4*)(mod + b * 6144 + 1024 + col); }
; #pragma unroll
;     for (int r = 0; r < 4; ++r) {
;       float ss = 0.f;
; #pragma unroll
;       for (int i = 0; i < 4; ++i) ss += v[r][i][0] * v[r][i][0] + v[r][i][1] * v[r][i][1] + v[r][i][2] * v[r][i][2] + v[r][i][3] * v[r][i][3];
;       ss = wave_sum(ss);
.LBB0_94:
	v_add_co_u32_e32 v0, vcc, 0xffffd000, v106
	v_ashrrev_i32_e32 v4, 13, v88
	s_nop 0
	v_addc_co_u32_e32 v1, vcc, -1, v107, vcc
	global_load_dwordx4 v[60:63], v[0:1], off offset:-3072
	global_load_dwordx4 v[56:59], v[0:1], off offset:-2048
	global_load_dwordx4 v[36:39], v[0:1], off offset:-1024
	global_load_dwordx4 v[32:35], v[0:1], off
	v_add_co_u32_e32 v0, vcc, 0xffffe000, v106
	v_mul_i32_i24_e32 v4, 0x1800, v4
	s_nop 0
	v_addc_co_u32_e32 v1, vcc, -1, v107, vcc
	global_load_dwordx4 v[52:55], v[0:1], off offset:-3072
	global_load_dwordx4 v[48:51], v[0:1], off offset:-2048
	global_load_dwordx4 v[44:47], v[0:1], off offset:-1024
	global_load_dwordx4 v[40:43], v[0:1], off
	v_ashrrev_i32_e32 v5, 31, v4
	v_lshl_add_u64 v[4:5], v[4:5], 2, s[20:21]
	v_lshl_add_u64 v[8:9], v[4:5], 0, s[24:25]
	v_mov_b32_e32 v109, v93
	v_mov_b32_e32 v111, v93
	v_mov_b32_e32 v113, v93
	v_lshl_add_u64 v[20:21], v[4:5], 0, v[92:93]
	v_lshl_add_u64 v[10:11], v[8:9], 0, v[92:93]
	global_load_dwordx4 v[0:3], v[94:95], off
	global_load_dwordx4 v[4:7], v[20:21], off
	v_lshl_add_u64 v[12:13], v[8:9], 0, v[108:109]
	v_lshl_add_u64 v[14:15], v[8:9], 0, v[110:111]
	v_lshl_add_u64 v[8:9], v[8:9], 0, v[112:113]
	global_load_dwordx4 v[72:75], v[10:11], off
	global_load_dwordx4 v[76:79], v[12:13], off
	global_load_dwordx4 v[68:71], v[14:15], off
	global_load_dwordx4 v[64:67], v[8:9], off
	v_add_co_u32_e32 v152, vcc, 0xfffff000, v106
	v_mov_b64_e32 v[126:127], s[28:29]
	s_nop 0
	v_addc_co_u32_e32 v153, vcc, -1, v107, vcc
	v_lshl_add_u64 v[134:135], s[84:85], 0, v[104:105]
	s_waitcnt vmcnt(13)
	v_mov_b32_e32 v10, v61
	s_waitcnt vmcnt(12)
	v_mov_b32_e32 v11, v57
	s_waitcnt vmcnt(11)
	v_mov_b32_e32 v18, v37
	s_waitcnt vmcnt(10)
	v_mov_b32_e32 v19, v33
	v_mov_b32_e32 v8, v60
	v_mov_b32_e32 v9, v56
	v_mov_b32_e32 v16, v36
	v_mov_b32_e32 v17, v32
	v_pk_mul_f32 v[10:11], v[10:11], v[10:11]
	v_pk_mul_f32 v[18:19], v[18:19], v[18:19]
	s_waitcnt vmcnt(9)
	v_mov_b32_e32 v28, v53
	s_waitcnt vmcnt(8)
	v_mov_b32_e32 v29, v49
	v_mov_b32_e32 v12, v62
	v_mov_b32_e32 v13, v58
	v_mov_b32_e32 v26, v52
	v_mov_b32_e32 v27, v48
	s_waitcnt vmcnt(7)
	v_mov_b32_e32 v84, v45
	s_waitcnt vmcnt(6)
	v_mov_b32_e32 v85, v41
	v_pk_fma_f32 v[8:9], v[8:9], v[8:9], v[10:11]
	v_pk_fma_f32 v[10:11], v[16:17], v[16:17], v[18:19]
	v_pk_mul_f32 v[16:17], v[28:29], v[28:29]
	v_mov_b32_e32 v30, v54
	v_mov_b32_e32 v31, v50
	v_mov_b32_e32 v82, v44
	v_mov_b32_e32 v83, v40
	v_pk_mul_f32 v[18:19], v[84:85], v[84:85]
	v_pk_fma_f32 v[8:9], v[12:13], v[12:13], v[8:9]
	v_pk_fma_f32 v[12:13], v[26:27], v[26:27], v[16:17]
	v_mov_b32_e32 v14, v63
	v_mov_b32_e32 v15, v59
	v_mov_b32_e32 v22, v38
	v_mov_b32_e32 v23, v34
	v_mov_b32_e32 v80, v55
	v_mov_b32_e32 v81, v51
	v_mov_b32_e32 v86, v46
	v_mov_b32_e32 v87, v42
	v_pk_fma_f32 v[16:17], v[82:83], v[82:83], v[18:19]
	v_pk_fma_f32 v[12:13], v[30:31], v[30:31], v[12:13]
	v_mov_b32_e32 v24, v39
	v_mov_b32_e32 v25, v35
	v_mov_b32_e32 v116, v47
	v_mov_b32_e32 v117, v43
	v_pk_fma_f32 v[10:11], v[22:23], v[22:23], v[10:11]
	v_pk_fma_f32 v[8:9], v[14:15], v[14:15], v[8:9]
	v_pk_fma_f32 v[14:15], v[86:87], v[86:87], v[16:17]
	v_pk_fma_f32 v[12:13], v[80:81], v[80:81], v[12:13]
	v_pk_fma_f32 v[10:11], v[24:25], v[24:25], v[10:11]
	v_pk_fma_f32 v[14:15], v[116:117], v[116:117], v[14:15]
	v_mov_b32_e32 v17, v8
	v_mov_b32_e32 v16, v12
	v_mov_b32_e32 v8, v13
	v_mov_b32_e32 v12, v14
	v_pk_add_f32 v[8:9], v[16:17], v[8:9]
	v_mov_b32_e32 v13, v10
	v_pk_add_f32 v[8:9], v[8:9], v[12:13]
	v_mov_b32_e32 v10, v15
	v_pk_add_f32 v[8:9], v[8:9], v[10:11]
	ds_bpermute_b32 v11, v91, v9
	ds_bpermute_b32 v10, v91, v8
	s_waitcnt vmcnt(3)
	v_pk_add_f32 v[122:123], v[74:75], 1.0 op_sel_hi:[1,0]
	s_waitcnt vmcnt(1)
	v_pk_add_f32 v[116:117], v[70:71], 1.0 op_sel_hi:[1,0]
	v_pk_add_f32 v[124:125], v[72:73], 1.0 op_sel_hi:[1,0]
	v_pk_add_f32 v[118:119], v[78:79], 1.0 op_sel_hi:[1,0]
	s_waitcnt lgkmcnt(0)
	v_pk_add_f32 v[8:9], v[8:9], v[10:11]
	ds_bpermute_b32 v11, v136, v9
	ds_bpermute_b32 v10, v136, v8
	v_pk_add_f32 v[120:121], v[76:77], 1.0 op_sel_hi:[1,0]
	s_waitcnt vmcnt(0)
	v_pk_add_f32 v[130:131], v[64:65], 1.0 op_sel_hi:[1,0]
	v_pk_add_f32 v[132:133], v[68:69], 1.0 op_sel_hi:[1,0]
	v_pk_add_f32 v[128:129], v[66:67], 1.0 op_sel_hi:[1,0]
	s_waitcnt lgkmcnt(0)
	v_pk_add_f32 v[22:23], v[8:9], v[10:11]
	ds_bpermute_b32 v25, v137, v23
	ds_bpermute_b32 v24, v137, v22
	global_load_dwordx4 v[16:19], v[94:95], off offset:1024
	global_load_dwordx4 v[12:15], v[94:95], off offset:2048
	global_load_dwordx4 v[8:11], v[94:95], off offset:3072
	global_load_dwordx4 v[28:31], v[20:21], off offset:1024
	s_waitcnt lgkmcnt(0)
	v_pk_add_f32 v[22:23], v[22:23], v[24:25]
	ds_bpermute_b32 v81, v138, v23
	ds_bpermute_b32 v80, v138, v22
	global_load_dwordx4 v[24:27], v[20:21], off offset:2048
	s_waitcnt lgkmcnt(0)
	v_pk_add_f32 v[80:81], v[22:23], v[80:81]
	ds_bpermute_b32 v83, v139, v81
	ds_bpermute_b32 v82, v139, v80
	global_load_dwordx4 v[20:23], v[20:21], off offset:3072
	s_waitcnt lgkmcnt(0)
	v_pk_add_f32 v[74:75], v[80:81], v[82:83]
	ds_bpermute_b32 v81, v140, v75
	ds_bpermute_b32 v80, v140, v74
	s_waitcnt lgkmcnt(0)
; DI unsigned pk2(float lo, float hi) { f32x2 v = {lo, hi}; bf16x2_t b = __builtin_convertvector(v, bf16x2_t); return __builtin_bit_cast(unsigned, b); }
; DI void phase_xnorm(const Params& p, int bid, int nb, char* lds) {
;     ...
;     for (int r = 0; r < 4; ++r) {
;       float ss = 0.f;
; #pragma unroll
;       for (int i = 0; i < 4; ++i) ss += v[r][i][0] * v[r][i][0] + v[r][i][1] * v[r][i][1] + v[r][i][2] * v[r][i][2] + v[r][i][3] * v[r][i][3];
;       ss = wave_sum(ss);
;       const float rstd = rsqrtf(ss * (1.f / 1024.f) + 1e-6f);
; #pragma unroll
;       for (int i = 0; i < 4; ++i) {
;         const f32x4 y = (v[r][i] * rstd * g4[i]) * (1.f + sc[i]) + sh[i];
;         u32x2 o = {pk2(y[0], y[1]), pk2(y[2], y[3])};
;         *(u32x2*)(h + (size_t)(row0 + r) * 1024 + 4 * lane + 256 * i) = o;
;         *(u32x2*)(yt + r * WP + 2 * (4 * lane + 256 * i)) = o;
;       }
	v_pk_add_f32 v[70:71], v[74:75], v[80:81]
	s_nop 0
	v_pk_fma_f32 v[154:155], v[70:71], s[26:27], v[126:127] op_sel_hi:[1,0,0]
	global_load_dwordx4 v[84:87], v[152:153], off offset:-3072
	global_load_dwordx4 v[80:83], v[152:153], off offset:-2048
	v_mul_f32_e32 v70, 0x4b800000, v155
	v_cmp_gt_f32_e32 vcc, s2, v155
	global_load_dwordx4 v[76:79], v[152:153], off offset:-1024
	global_load_dwordx4 v[72:75], v[106:107], off offset:-4096
	v_cndmask_b32_e32 v70, v155, v70, vcc
	v_rsq_f32_e32 v70, v70
	v_mul_f32_e32 v109, 0x4b800000, v154
	v_mul_f32_e32 v64, 0x45800000, v70
	v_cndmask_b32_e32 v156, v70, v64, vcc
	v_pk_mul_f32 v[62:63], v[62:63], v[156:157] op_sel_hi:[1,0]
	v_pk_mul_f32 v[60:61], v[60:61], v[156:157] op_sel_hi:[1,0]
	global_load_dwordx4 v[68:71], v[106:107], off offset:-3072
	global_load_dwordx4 v[64:67], v[106:107], off offset:-2048
	v_pk_mul_f32 v[60:61], v[0:1], v[60:61]
	v_pk_mul_f32 v[62:63], v[2:3], v[62:63]
	v_pk_fma_f32 v[60:61], v[124:125], v[60:61], v[4:5]
	v_pk_fma_f32 v[62:63], v[122:123], v[62:63], v[6:7]
	v_cvt_pk_bf16_f32 v152, v60, v61
	v_cvt_pk_bf16_f32 v153, v62, v63
	v_pk_mul_f32 v[160:161], v[58:59], v[156:157] op_sel_hi:[1,0]
	v_pk_mul_f32 v[162:163], v[56:57], v[156:157] op_sel_hi:[1,0]
	global_load_dwordx4 v[60:63], v[106:107], off offset:-1024
	global_load_dwordx4 v[56:59], v[106:107], off
	v_add_co_u32_e32 v158, vcc, s3, v134
	v_pk_mul_f32 v[34:35], v[34:35], v[156:157] op_sel_hi:[1,0]
	s_nop 0
	v_addc_co_u32_e32 v159, vcc, 0, v135, vcc
	v_add_co_u32_e32 v134, vcc, s11, v134
	v_pk_mul_f32 v[32:33], v[32:33], v[156:157] op_sel_hi:[1,0]
	s_nop 0
	v_addc_co_u32_e32 v135, vcc, 0, v135, vcc
	v_cmp_gt_f32_e32 vcc, s2, v154
	v_pk_mul_f32 v[38:39], v[38:39], v[156:157] op_sel_hi:[1,0]
	v_pk_mul_f32 v[36:37], v[36:37], v[156:157] op_sel_hi:[1,0]
	v_cndmask_b32_e32 v109, v154, v109, vcc
	v_rsq_f32_e32 v109, v109
	global_store_dwordx2 v[134:135], v[152:153], off offset:-4096
	v_mul_f32_e32 v111, 0x45800000, v109
	v_cndmask_b32_e32 v154, v109, v111, vcc
	v_add_u32_e32 v109, v90, v141
	v_pk_mul_f32 v[54:55], v[54:55], v[154:155] op_sel_hi:[1,0]
	v_pk_mul_f32 v[52:53], v[52:53], v[154:155] op_sel_hi:[1,0]
	v_pk_mul_f32 v[50:51], v[50:51], v[154:155] op_sel_hi:[1,0]
	v_pk_mul_f32 v[48:49], v[48:49], v[154:155] op_sel_hi:[1,0]
	v_pk_mul_f32 v[46:47], v[46:47], v[154:155] op_sel_hi:[1,0]
	v_pk_mul_f32 v[44:45], v[44:45], v[154:155] op_sel_hi:[1,0]
	v_pk_mul_f32 v[42:43], v[42:43], v[154:155] op_sel_hi:[1,0]
	v_pk_mul_f32 v[40:41], v[40:41], v[154:155] op_sel_hi:[1,0]
	s_waitcnt vmcnt(13)
	v_pk_mul_f32 v[36:37], v[12:13], v[36:37]
	s_waitcnt vmcnt(12)
	v_pk_mul_f32 v[32:33], v[8:9], v[32:33]
	v_pk_mul_f32 v[34:35], v[10:11], v[34:35]
	v_pk_mul_f32 v[38:39], v[14:15], v[38:39]
	ds_write_b64 v109, v[152:153] offset:33024
	v_pk_mul_f32 v[152:153], v[16:17], v[162:163]
	v_pk_mul_f32 v[154:155], v[18:19], v[160:161]
	s_waitcnt vmcnt(11)
	v_pk_fma_f32 v[152:153], v[120:121], v[152:153], v[28:29]
	s_waitcnt vmcnt(10)
	v_pk_fma_f32 v[38:39], v[116:117], v[38:39], v[26:27]
	v_pk_fma_f32 v[36:37], v[132:133], v[36:37], v[24:25]
	v_pk_fma_f32 v[154:155], v[118:119], v[154:155], v[30:31]
	v_cvt_pk_bf16_f32 v36, v36, v37
	v_cvt_pk_bf16_f32 v37, v38, v39
	global_store_dwordx2 v[158:159], v[36:37], off offset:1024
	ds_write_b64 v142, v[36:37] offset:33024
	s_waitcnt vmcnt(10)
	v_pk_fma_f32 v[34:35], v[128:129], v[34:35], v[22:23]
	v_pk_fma_f32 v[32:33], v[130:131], v[32:33], v[20:21]
	v_cvt_pk_bf16_f32 v152, v152, v153
	v_cvt_pk_bf16_f32 v32, v32, v33
	v_cvt_pk_bf16_f32 v33, v34, v35
	global_store_dwordx2 v[158:159], v[32:33], off offset:1536
	ds_write_b64 v143, v[32:33] offset:33024
	v_cvt_pk_bf16_f32 v153, v154, v155
	global_store_dwordx2 v[158:159], v[152:153], off offset:512
	ds_write_b64 v89, v[152:153] offset:33024
	s_waitcnt vmcnt(11)
	v_mov_b32_e32 v34, v85
	s_waitcnt vmcnt(10)
	v_mov_b32_e32 v35, v81
	v_mov_b32_e32 v32, v84
	v_mov_b32_e32 v33, v80
	v_pk_mul_f32 v[34:35], v[34:35], v[34:35]
	s_waitcnt vmcnt(9)
	v_mov_b32_e32 v36, v77
	v_pk_fma_f32 v[32:33], v[32:33], v[32:33], v[34:35]
	v_mov_b32_e32 v34, v86
	v_mov_b32_e32 v35, v82
	v_pk_fma_f32 v[32:33], v[34:35], v[34:35], v[32:33]
	v_mov_b32_e32 v34, v87
	v_mov_b32_e32 v35, v83
	s_waitcnt vmcnt(8)
	v_mov_b32_e32 v37, v73
	v_pk_fma_f32 v[32:33], v[34:35], v[34:35], v[32:33]
	v_mov_b32_e32 v34, v76
	v_mov_b32_e32 v35, v72
	v_pk_mul_f32 v[36:37], v[36:37], v[36:37]
	s_waitcnt vmcnt(7)
	v_mov_b32_e32 v38, v69
	v_pk_fma_f32 v[34:35], v[34:35], v[34:35], v[36:37]
	v_mov_b32_e32 v36, v78
	v_mov_b32_e32 v37, v74
	v_pk_fma_f32 v[34:35], v[36:37], v[36:37], v[34:35]
	v_mov_b32_e32 v36, v79
	v_mov_b32_e32 v37, v75
	s_waitcnt vmcnt(6)
	v_mov_b32_e32 v39, v65
	v_pk_fma_f32 v[34:35], v[36:37], v[36:37], v[34:35]
	v_mov_b32_e32 v36, v68
	v_mov_b32_e32 v37, v64
	v_pk_mul_f32 v[38:39], v[38:39], v[38:39]
	s_waitcnt vmcnt(5)
	v_mov_b32_e32 v152, v61
	v_pk_fma_f32 v[36:37], v[36:37], v[36:37], v[38:39]
	v_mov_b32_e32 v38, v70
	v_mov_b32_e32 v39, v66
	v_pk_fma_f32 v[36:37], v[38:39], v[38:39], v[36:37]
	v_mov_b32_e32 v38, v71
	v_mov_b32_e32 v39, v67
	s_waitcnt vmcnt(4)
	v_mov_b32_e32 v153, v57
	v_pk_fma_f32 v[36:37], v[38:39], v[38:39], v[36:37]
	v_mov_b32_e32 v38, v60
	v_mov_b32_e32 v39, v56
	v_pk_mul_f32 v[152:153], v[152:153], v[152:153]
	s_nop 0
	v_pk_fma_f32 v[38:39], v[38:39], v[38:39], v[152:153]
	v_mov_b32_e32 v152, v62
	v_mov_b32_e32 v153, v58
	v_pk_fma_f32 v[38:39], v[152:153], v[152:153], v[38:39]
	v_mov_b32_e32 v152, v63
	v_mov_b32_e32 v153, v59
	v_pk_fma_f32 v[38:39], v[152:153], v[152:153], v[38:39]
	v_mov_b32_e32 v152, v36
	v_mov_b32_e32 v153, v32
	v_mov_b32_e32 v32, v37
	v_pk_add_f32 v[32:33], v[152:153], v[32:33]
	v_mov_b32_e32 v36, v38
	v_mov_b32_e32 v37, v34
	v_pk_add_f32 v[32:33], v[32:33], v[36:37]
	v_mov_b32_e32 v34, v39
	v_pk_add_f32 v[32:33], v[32:33], v[34:35]
	ds_bpermute_b32 v35, v91, v33
	ds_bpermute_b32 v34, v91, v32
	v_pk_mul_f32 v[36:37], v[0:1], v[52:53]
	v_pk_mul_f32 v[38:39], v[2:3], v[54:55]
	v_pk_fma_f32 v[36:37], v[124:125], v[36:37], v[4:5]
	v_pk_fma_f32 v[38:39], v[122:123], v[38:39], v[6:7]
	s_waitcnt lgkmcnt(0)
; DI unsigned pk2(float lo, float hi) { f32x2 v = {lo, hi}; bf16x2_t b = __builtin_convertvector(v, bf16x2_t); return __builtin_bit_cast(unsigned, b); }
; DI void phase_xnorm(const Params& p, int bid, int nb, char* lds) {
;     ...
;     for (int r = 0; r < 4; ++r) {
;       float ss = 0.f;
; #pragma unroll
;       for (int i = 0; i < 4; ++i) ss += v[r][i][0] * v[r][i][0] + v[r][i][1] * v[r][i][1] + v[r][i][2] * v[r][i][2] + v[r][i][3] * v[r][i][3];
;       ss = wave_sum(ss);
;       const float rstd = rsqrtf(ss * (1.f / 1024.f) + 1e-6f);
; #pragma unroll
;       for (int i = 0; i < 4; ++i) {
;         const f32x4 y = (v[r][i] * rstd * g4[i]) * (1.f + sc[i]) + sh[i];
;         u32x2 o = {pk2(y[0], y[1]), pk2(y[2], y[3])};
;         *(u32x2*)(h + (size_t)(row0 + r) * 1024 + 4 * lane + 256 * i) = o;
;         *(u32x2*)(yt + r * WP + 2 * (4 * lane + 256 * i)) = o;
;       }
	v_pk_add_f32 v[32:33], v[32:33], v[34:35]
	ds_bpermute_b32 v35, v136, v33
	ds_bpermute_b32 v34, v136, v32
	v_cvt_pk_bf16_f32 v36, v36, v37
	v_cvt_pk_bf16_f32 v37, v38, v39
	global_store_dwordx2 v[158:159], v[36:37], off offset:2048
	ds_write_b64 v109, v[36:37] offset:35088
	s_waitcnt lgkmcnt(1)
	v_pk_add_f32 v[32:33], v[32:33], v[34:35]
	ds_bpermute_b32 v35, v137, v33
	ds_bpermute_b32 v34, v137, v32
	v_pk_mul_f32 v[36:37], v[16:17], v[48:49]
	v_pk_mul_f32 v[38:39], v[18:19], v[50:51]
	v_pk_fma_f32 v[36:37], v[120:121], v[36:37], v[28:29]
	v_pk_fma_f32 v[38:39], v[118:119], v[38:39], v[30:31]
	s_waitcnt lgkmcnt(0)
	v_pk_add_f32 v[32:33], v[32:33], v[34:35]
	ds_bpermute_b32 v35, v138, v33
	ds_bpermute_b32 v34, v138, v32
	v_cvt_pk_bf16_f32 v36, v36, v37
	v_cvt_pk_bf16_f32 v37, v38, v39
	global_store_dwordx2 v[158:159], v[36:37], off offset:2560
	ds_write_b64 v89, v[36:37] offset:35088
	s_waitcnt lgkmcnt(1)
	v_pk_add_f32 v[32:33], v[32:33], v[34:35]
	ds_bpermute_b32 v35, v139, v33
	ds_bpermute_b32 v34, v139, v32
	v_pk_mul_f32 v[36:37], v[12:13], v[44:45]
	v_pk_mul_f32 v[38:39], v[14:15], v[46:47]
	v_pk_fma_f32 v[36:37], v[132:133], v[36:37], v[24:25]
	v_pk_fma_f32 v[38:39], v[116:117], v[38:39], v[26:27]
	s_waitcnt lgkmcnt(0)
	v_pk_add_f32 v[32:33], v[32:33], v[34:35]
	ds_bpermute_b32 v35, v140, v33
	ds_bpermute_b32 v34, v140, v32
	v_cvt_pk_bf16_f32 v36, v36, v37
	v_cvt_pk_bf16_f32 v37, v38, v39
	global_store_dwordx2 v[158:159], v[36:37], off offset:3072
	ds_write_b64 v142, v[36:37] offset:35088
	s_waitcnt lgkmcnt(1)
	v_pk_add_f32 v[32:33], v[32:33], v[34:35]
	v_pk_mul_f32 v[34:35], v[8:9], v[40:41]
	v_pk_fma_f32 v[32:33], v[32:33], s[26:27], v[126:127] op_sel_hi:[1,0,0]
	v_pk_fma_f32 v[34:35], v[130:131], v[34:35], v[20:21]
	v_cmp_gt_f32_e32 vcc, s2, v33
	v_cvt_pk_bf16_f32 v34, v34, v35
	v_mul_f32_e32 v35, 0x4b800000, v33
	v_cndmask_b32_e32 v33, v33, v35, vcc
	v_rsq_f32_e32 v33, v33
	v_pk_mul_f32 v[36:37], v[10:11], v[42:43]
	s_nop 0
	v_pk_fma_f32 v[36:37], v[128:129], v[36:37], v[22:23]
	s_nop 0
	v_cvt_pk_bf16_f32 v35, v36, v37
	global_store_dwordx2 v[158:159], v[34:35], off offset:3584
	ds_write_b64 v143, v[34:35] offset:35088
	v_mul_f32_e32 v34, 0x45800000, v33
	v_cndmask_b32_e32 v34, v33, v34, vcc
	v_pk_mul_f32 v[36:37], v[86:87], v[34:35] op_sel_hi:[1,0]
	v_pk_mul_f32 v[38:39], v[84:85], v[34:35] op_sel_hi:[1,0]
	v_pk_mul_f32 v[36:37], v[2:3], v[36:37]
	v_pk_mul_f32 v[38:39], v[0:1], v[38:39]
	v_pk_fma_f32 v[36:37], v[122:123], v[36:37], v[6:7]
	v_pk_fma_f32 v[38:39], v[124:125], v[38:39], v[4:5]
	v_mul_f32_e32 v33, 0x4b800000, v32
	v_cvt_pk_bf16_f32 v38, v38, v39
	v_cvt_pk_bf16_f32 v39, v36, v37
	global_store_dwordx2 v[134:135], v[38:39], off
	ds_write_b64 v109, v[38:39] offset:37152
	v_pk_mul_f32 v[36:37], v[82:83], v[34:35] op_sel_hi:[1,0]
	v_pk_mul_f32 v[38:39], v[80:81], v[34:35] op_sel_hi:[1,0]
	v_pk_mul_f32 v[36:37], v[18:19], v[36:37]
	v_pk_mul_f32 v[38:39], v[16:17], v[38:39]
	v_pk_fma_f32 v[36:37], v[118:119], v[36:37], v[30:31]
	v_pk_fma_f32 v[38:39], v[120:121], v[38:39], v[28:29]
	v_cmp_gt_f32_e32 vcc, s2, v32
	v_cvt_pk_bf16_f32 v38, v38, v39
	v_cvt_pk_bf16_f32 v39, v36, v37
	global_store_dwordx2 v[134:135], v[38:39], off offset:512
	ds_write_b64 v89, v[38:39] offset:37152
	v_pk_mul_f32 v[36:37], v[78:79], v[34:35] op_sel_hi:[1,0]
	v_pk_mul_f32 v[38:39], v[76:77], v[34:35] op_sel_hi:[1,0]
	v_cndmask_b32_e32 v32, v32, v33, vcc
	v_pk_mul_f32 v[38:39], v[12:13], v[38:39]
	v_pk_mul_f32 v[36:37], v[14:15], v[36:37]
	v_rsq_f32_e32 v32, v32
	v_pk_fma_f32 v[36:37], v[116:117], v[36:37], v[26:27]
	v_pk_fma_f32 v[38:39], v[132:133], v[38:39], v[24:25]
	v_mul_f32_e32 v33, 0x45800000, v32
	v_cvt_pk_bf16_f32 v38, v38, v39
	v_cvt_pk_bf16_f32 v39, v36, v37
	v_pk_mul_f32 v[36:37], v[74:75], v[34:35] op_sel_hi:[1,0]
	v_pk_mul_f32 v[34:35], v[72:73], v[34:35] op_sel_hi:[1,0]
	v_pk_mul_f32 v[36:37], v[10:11], v[36:37]
	v_pk_mul_f32 v[34:35], v[8:9], v[34:35]
	v_pk_fma_f32 v[36:37], v[128:129], v[36:37], v[22:23]
	v_pk_fma_f32 v[34:35], v[130:131], v[34:35], v[20:21]
	v_cndmask_b32_e32 v32, v32, v33, vcc
	v_cvt_pk_bf16_f32 v34, v34, v35
	v_cvt_pk_bf16_f32 v35, v36, v37
	global_store_dwordx2 v[134:135], v[34:35], off offset:1536
	ds_write_b64 v143, v[34:35] offset:37152
	v_pk_mul_f32 v[34:35], v[70:71], v[32:33] op_sel_hi:[1,0]
	v_pk_mul_f32 v[36:37], v[68:69], v[32:33] op_sel_hi:[1,0]
	v_pk_mul_f32 v[2:3], v[2:3], v[34:35]
	v_pk_mul_f32 v[0:1], v[0:1], v[36:37]
	v_pk_fma_f32 v[2:3], v[122:123], v[2:3], v[6:7]
	v_pk_fma_f32 v[0:1], v[124:125], v[0:1], v[4:5]
	global_store_dwordx2 v[134:135], v[38:39], off offset:1024
	v_cvt_pk_bf16_f32 v0, v0, v1
	v_cvt_pk_bf16_f32 v1, v2, v3
	global_store_dwordx2 v[134:135], v[0:1], off offset:2048
	ds_write_b64 v109, v[0:1] offset:39216
	v_pk_mul_f32 v[0:1], v[66:67], v[32:33] op_sel_hi:[1,0]
	v_pk_mul_f32 v[2:3], v[64:65], v[32:33] op_sel_hi:[1,0]
	v_pk_mul_f32 v[0:1], v[18:19], v[0:1]
	v_pk_mul_f32 v[2:3], v[16:17], v[2:3]
	v_pk_fma_f32 v[0:1], v[118:119], v[0:1], v[30:31]
	v_pk_fma_f32 v[2:3], v[120:121], v[2:3], v[28:29]
	ds_write_b64 v142, v[38:39] offset:37152
	v_cvt_pk_bf16_f32 v2, v2, v3
	v_cvt_pk_bf16_f32 v3, v0, v1
	global_store_dwordx2 v[134:135], v[2:3], off offset:2560
	ds_write_b64 v89, v[2:3] offset:39216
	v_pk_mul_f32 v[0:1], v[62:63], v[32:33] op_sel_hi:[1,0]
	v_pk_mul_f32 v[2:3], v[60:61], v[32:33] op_sel_hi:[1,0]
	v_pk_mul_f32 v[0:1], v[14:15], v[0:1]
	v_pk_mul_f32 v[2:3], v[12:13], v[2:3]
	v_pk_fma_f32 v[0:1], v[116:117], v[0:1], v[26:27]
	v_pk_fma_f32 v[2:3], v[132:133], v[2:3], v[24:25]
	s_nop 0
	v_cvt_pk_bf16_f32 v2, v2, v3
	v_cvt_pk_bf16_f32 v3, v0, v1
	global_store_dwordx2 v[134:135], v[2:3], off offset:3072
	ds_write_b64 v142, v[2:3] offset:39216
	v_pk_mul_f32 v[0:1], v[58:59], v[32:33] op_sel_hi:[1,0]
	v_pk_mul_f32 v[2:3], v[56:57], v[32:33] op_sel_hi:[1,0]
	v_pk_mul_f32 v[0:1], v[10:11], v[0:1]
	v_pk_mul_f32 v[2:3], v[8:9], v[2:3]
	v_pk_fma_f32 v[0:1], v[128:129], v[0:1], v[22:23]
	v_pk_fma_f32 v[2:3], v[130:131], v[2:3], v[20:21]
	s_nop 0
	v_cvt_pk_bf16_f32 v2, v2, v3
	v_cvt_pk_bf16_f32 v3, v0, v1
	global_store_dwordx2 v[134:135], v[2:3], off offset:3584
	ds_write_b64 v143, v[2:3] offset:39216
	ds_read_b128 v[0:3], v144 offset:33024
	ds_read_b128 v[4:7], v144 offset:33088
	ds_read_b128 v[8:11], v145
	ds_read_b128 v[12:15], v145 offset:64
	s_waitcnt lgkmcnt(1)
; #define MFMA16(a, b, c) __builtin_amdgcn_mfma_f32_16x16x32_bf16((a), (b), (c), 0, 0, 0)
; DI void phase_xnorm(const Params& p, int bid, int nb, char* lds) {
;     ...
;     f32x4 acc = {0.f, 0.f, 0.f, 0.f};
;     const char* ya = yt + (fr & 3) * WP + fq * 16; const char* wb = w16 + fr * WP + fq * 16;
; #pragma unroll
;     for (int kb = 0; kb < 4; ++kb) {
;       bf16x8 fa[8], fb[8];
; #pragma unroll
;       for (int q = 0; q < 8; ++q) { fa[q] = *(const bf16x8*)(ya + (8 * kb + q) * 64); fb[q] = *(const bf16x8*)(wb + (8 * kb + q) * 64); }
; #pragma unroll
;       for (int q = 0; q < 8; ++q) acc = MFMA16(fa[q], fb[q], acc);
;     }
;     asm volatile("" ::: "memory");
;     if (fq == 0) {
	v_mfma_f32_16x16x32_bf16 v[0:3], v[0:3], v[8:11], 0
	ds_read_b128 v[8:11], v144 offset:33152
	ds_read_b128 v[16:19], v144 offset:33216
	s_waitcnt lgkmcnt(2)
	v_mfma_f32_16x16x32_bf16 v[0:3], v[4:7], v[12:15], v[0:3]
	ds_read_b128 v[4:7], v145 offset:128
	ds_read_b128 v[12:15], v145 offset:192
	s_waitcnt lgkmcnt(1)
	v_mfma_f32_16x16x32_bf16 v[0:3], v[8:11], v[4:7], v[0:3]
	ds_read_b128 v[4:7], v144 offset:33280
	ds_read_b128 v[8:11], v144 offset:33344
	s_waitcnt lgkmcnt(2)
	v_mfma_f32_16x16x32_bf16 v[0:3], v[16:19], v[12:15], v[0:3]
	ds_read_b128 v[12:15], v145 offset:256
	ds_read_b128 v[16:19], v145 offset:320
	s_waitcnt lgkmcnt(1)
	v_mfma_f32_16x16x32_bf16 v[0:3], v[4:7], v[12:15], v[0:3]
	ds_read_b128 v[4:7], v144 offset:33408
	ds_read_b128 v[12:15], v144 offset:33472
	s_waitcnt lgkmcnt(2)
	v_mfma_f32_16x16x32_bf16 v[0:3], v[8:11], v[16:19], v[0:3]
	ds_read_b128 v[8:11], v145 offset:384
	ds_read_b128 v[16:19], v145 offset:448
	s_waitcnt lgkmcnt(1)
	v_mfma_f32_16x16x32_bf16 v[0:3], v[4:7], v[8:11], v[0:3]
	ds_read_b128 v[4:7], v144 offset:33536
	s_waitcnt lgkmcnt(1)
	v_mfma_f32_16x16x32_bf16 v[0:3], v[12:15], v[16:19], v[0:3]
	ds_read_b128 v[8:11], v144 offset:33600
	ds_read_b128 v[12:15], v145 offset:512
	ds_read_b128 v[16:19], v145 offset:576
	s_waitcnt lgkmcnt(1)
	v_mfma_f32_16x16x32_bf16 v[0:3], v[4:7], v[12:15], v[0:3]
	ds_read_b128 v[4:7], v144 offset:33664
	ds_read_b128 v[12:15], v144 offset:33728
	s_waitcnt lgkmcnt(2)
	v_mfma_f32_16x16x32_bf16 v[0:3], v[8:11], v[16:19], v[0:3]
	ds_read_b128 v[8:11], v145 offset:640
	ds_read_b128 v[16:19], v145 offset:704
	s_waitcnt lgkmcnt(1)
	v_mfma_f32_16x16x32_bf16 v[0:3], v[4:7], v[8:11], v[0:3]
	ds_read_b128 v[4:7], v144 offset:33792
	ds_read_b128 v[8:11], v144 offset:33856
	s_waitcnt lgkmcnt(2)
	v_mfma_f32_16x16x32_bf16 v[0:3], v[12:15], v[16:19], v[0:3]
	ds_read_b128 v[12:15], v145 offset:768
	ds_read_b128 v[16:19], v145 offset:832
	s_waitcnt lgkmcnt(1)
	v_mfma_f32_16x16x32_bf16 v[0:3], v[4:7], v[12:15], v[0:3]
	ds_read_b128 v[4:7], v144 offset:33920
	ds_read_b128 v[12:15], v144 offset:33984
	s_waitcnt lgkmcnt(2)
	v_mfma_f32_16x16x32_bf16 v[0:3], v[8:11], v[16:19], v[0:3]
	ds_read_b128 v[8:11], v145 offset:896
	ds_read_b128 v[16:19], v145 offset:960
	s_waitcnt lgkmcnt(1)
	v_mfma_f32_16x16x32_bf16 v[0:3], v[4:7], v[8:11], v[0:3]
	ds_read_b128 v[4:7], v144 offset:34048
	s_waitcnt lgkmcnt(1)
	v_mfma_f32_16x16x32_bf16 v[0:3], v[12:15], v[16:19], v[0:3]
	ds_read_b128 v[8:11], v144 offset:34112
	ds_read_b128 v[12:15], v145 offset:1024
	ds_read_b128 v[16:19], v145 offset:1088
	s_waitcnt lgkmcnt(1)
	v_mfma_f32_16x16x32_bf16 v[0:3], v[4:7], v[12:15], v[0:3]
	ds_read_b128 v[4:7], v144 offset:34176
	ds_read_b128 v[12:15], v144 offset:34240
	s_waitcnt lgkmcnt(2)
	v_mfma_f32_16x16x32_bf16 v[0:3], v[8:11], v[16:19], v[0:3]
	ds_read_b128 v[8:11], v145 offset:1152
	ds_read_b128 v[16:19], v145 offset:1216
	s_waitcnt lgkmcnt(1)
	v_mfma_f32_16x16x32_bf16 v[0:3], v[4:7], v[8:11], v[0:3]
	ds_read_b128 v[4:7], v144 offset:34304
	ds_read_b128 v[8:11], v144 offset:34368
	s_waitcnt lgkmcnt(2)
	v_mfma_f32_16x16x32_bf16 v[0:3], v[12:15], v[16:19], v[0:3]
	ds_read_b128 v[12:15], v145 offset:1280
	ds_read_b128 v[16:19], v145 offset:1344
	s_waitcnt lgkmcnt(1)
	v_mfma_f32_16x16x32_bf16 v[0:3], v[4:7], v[12:15], v[0:3]
	ds_read_b128 v[4:7], v144 offset:34432
	ds_read_b128 v[12:15], v144 offset:34496
	s_waitcnt lgkmcnt(2)
	v_mfma_f32_16x16x32_bf16 v[0:3], v[8:11], v[16:19], v[0:3]
	ds_read_b128 v[8:11], v145 offset:1408
	ds_read_b128 v[16:19], v145 offset:1472
	s_waitcnt lgkmcnt(1)
	v_mfma_f32_16x16x32_bf16 v[0:3], v[4:7], v[8:11], v[0:3]
	ds_read_b128 v[4:7], v144 offset:34560
	s_waitcnt lgkmcnt(1)
	v_mfma_f32_16x16x32_bf16 v[0:3], v[12:15], v[16:19], v[0:3]
	ds_read_b128 v[8:11], v144 offset:34624
	ds_read_b128 v[12:15], v145 offset:1536
	ds_read_b128 v[16:19], v145 offset:1600
	s_waitcnt lgkmcnt(1)
	v_mfma_f32_16x16x32_bf16 v[0:3], v[4:7], v[12:15], v[0:3]
	ds_read_b128 v[4:7], v144 offset:34688
	ds_read_b128 v[12:15], v144 offset:34752
	s_waitcnt lgkmcnt(2)
	v_mfma_f32_16x16x32_bf16 v[0:3], v[8:11], v[16:19], v[0:3]
	ds_read_b128 v[8:11], v145 offset:1664
	ds_read_b128 v[16:19], v145 offset:1728
	s_waitcnt lgkmcnt(1)
	v_mfma_f32_16x16x32_bf16 v[0:3], v[4:7], v[8:11], v[0:3]
	ds_read_b128 v[4:7], v144 offset:34816
	ds_read_b128 v[8:11], v144 offset:34880
	s_waitcnt lgkmcnt(2)
	v_mfma_f32_16x16x32_bf16 v[0:3], v[12:15], v[16:19], v[0:3]
	ds_read_b128 v[12:15], v145 offset:1792
	ds_read_b128 v[16:19], v145 offset:1856
	s_waitcnt lgkmcnt(1)
	v_mfma_f32_16x16x32_bf16 v[0:3], v[4:7], v[12:15], v[0:3]
	ds_read_b128 v[4:7], v144 offset:34944
	ds_read_b128 v[12:15], v144 offset:35008
	s_waitcnt lgkmcnt(2)
	v_mfma_f32_16x16x32_bf16 v[0:3], v[8:11], v[16:19], v[0:3]
	ds_read_b128 v[8:11], v145 offset:1920
	ds_read_b128 v[16:19], v145 offset:1984
	s_waitcnt lgkmcnt(1)
	v_mfma_f32_16x16x32_bf16 v[0:3], v[4:7], v[8:11], v[0:3]
	s_waitcnt lgkmcnt(0)
	v_mfma_f32_16x16x32_bf16 v[0:3], v[12:15], v[16:19], v[0:3]
	s_and_saveexec_b64 s[30:31], s[4:5]
	s_cbranch_execz .LBB0_93
; DI float sigmoidf_(float x) { return __builtin_amdgcn_rcpf(1.f + __expf(-x)); }
; DI float softplusf_(float x) { return fmaxf(x, 0.f) + log1pf(__expf(-fabsf(x))); }
; DI void phase_xnorm(const Params& p, int bid, int nb, char* lds) {
;     ...
;       for (int r = 0; r < 4; ++r) { const float xx = acc[r]; float res;
;         if (j < 8) res = -softplusf_(-(xx + p.b_fgate[j]));
;         else if (j < 12) res = sigmoidf_(xx);
;         else res = -__expf(p.a_log[j - 12]) * softplusf_(xx + p.dt_bias[j - 12]);
;         small[(size_t)(row0 + r) * 16 + j] = res; }
	s_and_saveexec_b64 s[34:35], s[6:7]
	s_xor_b64 s[34:35], exec, s[34:35]
	s_cbranch_execz .LBB0_101
	s_and_saveexec_b64 s[38:39], s[8:9]
	s_xor_b64 s[38:39], exec, s[38:39]
	s_cbranch_execz .LBB0_98
	v_mov_b32_e32 v4, v240
	v_mov_b32_e32 v5, v241
	v_add_f32_e32 v4, v0, v4
	v_mul_f32_e64 v6, |v4|, s18
	v_exp_f32_e32 v18, v6
	v_mul_f32_e32 v5, 0x3fb8aa3b, v5
	v_exp_f32_e32 v19, v5
	v_max_f32_e32 v20, 0, v4
	v_add_f32_e32 v6, 1.0, v18
	v_add_f32_e32 v7, -1.0, v6
	v_frexp_mant_f32_e32 v8, v6
	v_cvt_f64_f32_e32 v[4:5], v6
	v_sub_f32_e32 v9, v7, v6
	v_frexp_exp_i32_f64_e32 v4, v[4:5]
	v_cmp_gt_f32_e32 vcc, s19, v8
	v_sub_f32_e32 v7, v18, v7
	v_add_f32_e32 v5, 1.0, v9
	v_subbrev_co_u32_e32 v4, vcc, 0, v4, vcc
	v_add_f32_e32 v5, v7, v5
	v_sub_u32_e32 v7, 0, v4
	v_ldexp_f32 v6, v6, v7
	v_add_f32_e32 v8, -1.0, v6
	v_add_f32_e32 v9, 1.0, v6
	v_ldexp_f32 v5, v5, v7
	v_add_f32_e32 v7, 1.0, v8
	v_add_f32_e32 v10, -1.0, v9
	v_sub_f32_e32 v7, v6, v7
	v_sub_f32_e32 v6, v6, v10
	v_add_f32_e32 v10, v5, v7
	v_add_f32_e32 v5, v5, v6
	v_add_f32_e32 v12, v9, v5
	v_rcp_f32_e32 v13, v12
	v_add_f32_e32 v7, v8, v10
	v_sub_f32_e32 v8, v7, v8
	v_sub_f32_e32 v6, v12, v9
	v_mul_f32_e32 v15, v7, v13
	v_sub_f32_e32 v14, v10, v8
	v_mul_f32_e32 v8, v12, v15
	v_sub_f32_e32 v5, v5, v6
	v_fma_f32 v10, v15, v12, -v8
	v_fmac_f32_e32 v10, v15, v5
	v_add_f32_e32 v6, v8, v10
	v_sub_f32_e32 v9, v7, v6
	v_mov_b32_e32 v11, v6
	v_pk_add_f32 v[6:7], v[6:7], v[8:9] neg_lo:[0,1] neg_hi:[0,1]
	v_cvt_f32_i32_e32 v4, v4
	v_pk_add_f32 v[6:7], v[6:7], v[10:11] neg_lo:[0,1] neg_hi:[0,1]
	v_cmp_neq_f32_e32 vcc, s29, v18
	v_add_f32_e32 v7, v14, v7
	v_add_f32_e32 v6, v6, v7
	v_add_f32_e32 v7, v9, v6
	v_mul_f32_e32 v11, v13, v7
	v_mul_f32_e32 v8, v12, v11
	v_sub_f32_e32 v9, v9, v7
	v_add_f32_e32 v16, v15, v11
	v_fma_f32 v10, v11, v12, -v8
	v_add_f32_e32 v14, v6, v9
	v_sub_f32_e32 v6, v16, v15
	v_fmac_f32_e32 v10, v11, v5
	v_sub_f32_e32 v5, v11, v6
	v_add_f32_e32 v6, v8, v10
	v_sub_f32_e32 v9, v7, v6
	v_mov_b32_e32 v11, v6
	v_pk_add_f32 v[6:7], v[6:7], v[8:9] neg_lo:[0,1] neg_hi:[0,1]
	s_nop 0
	v_pk_add_f32 v[6:7], v[6:7], v[10:11] neg_lo:[0,1] neg_hi:[0,1]
	s_nop 0
	v_add_f32_e32 v7, v14, v7
	v_add_f32_e32 v6, v6, v7
	v_add_f32_e32 v6, v9, v6
	v_mul_f32_e32 v6, v13, v6
	v_add_f32_e32 v5, v5, v6
	v_add_f32_e32 v6, v16, v5
	v_mul_f32_e32 v8, v6, v6
	v_sub_f32_e32 v9, v6, v16
	v_fmamk_f32 v10, v8, 0x3e9b6dac, v148
	v_sub_f32_e32 v9, v5, v9
	v_mul_f32_e32 v5, v6, v8
	v_fmaak_f32 v115, v8, v10, 0x3f2aaada
	v_ldexp_f32 v11, v9, 1
	v_pk_mul_f32 v[8:9], v[4:5], v[114:115]
	v_ldexp_f32 v7, v6, 1
	v_fma_f32 v6, v4, s27, -v8
	v_fmac_f32_e32 v6, 0xb102e308, v4
	v_pk_add_f32 v[4:5], v[8:9], v[6:7]
	v_mov_b32_e32 v10, v8
	v_sub_f32_e32 v14, v5, v7
	v_pk_add_f32 v[12:13], v[4:5], v[8:9] neg_lo:[0,1] neg_hi:[0,1]
	v_sub_f32_e32 v8, v9, v14
	v_add_f32_e32 v11, v11, v8
	v_pk_add_f32 v[8:9], v[4:5], v[10:11]
	v_mov_b32_e32 v7, v4
	v_mov_b32_e32 v13, v9
	v_pk_add_f32 v[16:17], v[6:7], v[12:13] neg_lo:[0,1] neg_hi:[0,1]
	v_pk_add_f32 v[6:7], v[6:7], v[12:13]
	v_mov_b32_e32 v15, v4
	v_pk_add_f32 v[12:13], v[6:7], v[4:5] op_sel:[1,0] op_sel_hi:[0,1] neg_lo:[0,1] neg_hi:[0,1]
	v_mov_b32_e32 v14, v11
	v_mov_b32_e32 v10, v9
	v_mov_b32_e32 v11, v7
	v_pk_mov_b32 v[4:5], v[4:5], v[12:13] op_sel:[1,0]
	v_pk_add_f32 v[8:9], v[8:9], v[12:13] op_sel_hi:[1,0] neg_lo:[0,1] neg_hi:[0,1]
	v_pk_add_f32 v[4:5], v[10:11], v[4:5] neg_lo:[0,1] neg_hi:[0,1]
	v_mov_b32_e32 v8, v16
	v_pk_add_f32 v[4:5], v[14:15], v[4:5] neg_lo:[0,1] neg_hi:[0,1]
	v_mov_b32_e32 v17, v7
	v_pk_add_f32 v[8:9], v[8:9], v[4:5]
	s_nop 0
	v_pk_add_f32 v[10:11], v[8:9], v[8:9] op_sel:[0,1] op_sel_hi:[1,0]
	s_nop 0
	v_pk_add_f32 v[6:7], v[6:7], v[10:11] op_sel:[1,0] op_sel_hi:[0,1]
	v_mov_b32_e32 v9, v6
	v_mov_b32_e32 v5, v10
	v_pk_add_f32 v[10:11], v[8:9], v[16:17] neg_lo:[0,1] neg_hi:[0,1]
	s_nop 0
	v_sub_f32_e32 v7, v8, v10
	v_pk_add_f32 v[4:5], v[4:5], v[10:11] neg_lo:[0,1] neg_hi:[0,1]
	v_sub_f32_e32 v7, v16, v7
	v_add_f32_e32 v4, v4, v7
	v_add_f32_e32 v4, v4, v5
	v_add_f32_e32 v4, v6, v4
	v_cndmask_b32_e32 v4, v149, v4, vcc
	v_cmp_ngt_f32_e32 vcc, -1.0, v18
	s_nop 1
	v_cndmask_b32_e32 v4, v150, v4, vcc
	v_cmp_neq_f32_e32 vcc, -1.0, v18
	s_nop 1
	v_cndmask_b32_e32 v4, v151, v4, vcc
	v_cmp_lt_f32_e64 vcc, |v18|, s40
	s_nop 1
	v_cndmask_b32_e32 v4, v4, v18, vcc
	v_add_f32_e32 v4, v20, v4
	v_mul_f32_e64 v6, v4, -v19

; DI float softplusf_(float x) { return fmaxf(x, 0.f) + log1pf(__expf(-fabsf(x))); }
; DI void phase_xnorm(const Params& p, int bid, int nb, char* lds) {
;     ...
;       for (int r = 0; r < 4; ++r) { const float xx = acc[r]; float res;
;         if (j < 8) res = -softplusf_(-(xx + p.b_fgate[j]));
.LBB0_101:
	s_andn2_saveexec_b64 s[34:35], s[34:35]
	s_cbranch_execz .LBB0_103
	v_mov_b32_e32 v4, v242
	v_add_f32_e32 v0, v0, v4
	v_mul_f32_e64 v4, |v0|, s18
	v_exp_f32_e32 v18, v4
	v_max_f32_e64 v0, -v0, 0
	v_add_f32_e32 v6, 1.0, v18
	v_add_f32_e32 v7, -1.0, v6
	v_frexp_mant_f32_e32 v8, v6
	v_cvt_f64_f32_e32 v[4:5], v6
	v_sub_f32_e32 v9, v7, v6
	v_frexp_exp_i32_f64_e32 v4, v[4:5]
	v_cmp_gt_f32_e32 vcc, s19, v8
	v_sub_f32_e32 v7, v18, v7
	v_add_f32_e32 v5, 1.0, v9
	v_subbrev_co_u32_e32 v4, vcc, 0, v4, vcc
	v_add_f32_e32 v5, v7, v5
	v_sub_u32_e32 v7, 0, v4
	v_ldexp_f32 v6, v6, v7
	v_add_f32_e32 v8, -1.0, v6
	v_add_f32_e32 v9, 1.0, v6
	v_ldexp_f32 v5, v5, v7
	v_add_f32_e32 v7, 1.0, v8
	v_add_f32_e32 v10, -1.0, v9
	v_sub_f32_e32 v7, v6, v7
	v_sub_f32_e32 v6, v6, v10
	v_add_f32_e32 v10, v5, v7
	v_add_f32_e32 v5, v5, v6
	v_add_f32_e32 v12, v9, v5
	v_rcp_f32_e32 v13, v12
	v_add_f32_e32 v7, v8, v10
	v_sub_f32_e32 v8, v7, v8
	v_sub_f32_e32 v6, v12, v9
	v_mul_f32_e32 v15, v7, v13
	v_sub_f32_e32 v14, v10, v8
	v_mul_f32_e32 v8, v12, v15
	v_sub_f32_e32 v5, v5, v6
	v_fma_f32 v10, v15, v12, -v8
	v_fmac_f32_e32 v10, v15, v5
	v_add_f32_e32 v6, v8, v10
	v_sub_f32_e32 v9, v7, v6
	v_mov_b32_e32 v11, v6
	v_pk_add_f32 v[6:7], v[6:7], v[8:9] neg_lo:[0,1] neg_hi:[0,1]
	v_cvt_f32_i32_e32 v4, v4
	v_pk_add_f32 v[6:7], v[6:7], v[10:11] neg_lo:[0,1] neg_hi:[0,1]
	v_cmp_neq_f32_e32 vcc, s29, v18
	v_add_f32_e32 v7, v14, v7
	v_add_f32_e32 v6, v6, v7
	v_add_f32_e32 v7, v9, v6
	v_mul_f32_e32 v11, v13, v7
	v_mul_f32_e32 v8, v12, v11
	v_sub_f32_e32 v9, v9, v7
	v_add_f32_e32 v16, v15, v11
	v_fma_f32 v10, v11, v12, -v8
	v_add_f32_e32 v14, v6, v9
	v_sub_f32_e32 v6, v16, v15
	v_fmac_f32_e32 v10, v11, v5
	v_sub_f32_e32 v5, v11, v6
	v_add_f32_e32 v6, v8, v10
	v_sub_f32_e32 v9, v7, v6
	v_mov_b32_e32 v11, v6
	v_pk_add_f32 v[6:7], v[6:7], v[8:9] neg_lo:[0,1] neg_hi:[0,1]
	s_nop 0
	v_pk_add_f32 v[6:7], v[6:7], v[10:11] neg_lo:[0,1] neg_hi:[0,1]
	s_nop 0
	v_add_f32_e32 v7, v14, v7
	v_add_f32_e32 v6, v6, v7
	v_add_f32_e32 v6, v9, v6
	v_mul_f32_e32 v6, v13, v6
	v_add_f32_e32 v5, v5, v6
	v_add_f32_e32 v6, v16, v5
	v_mul_f32_e32 v8, v6, v6
	v_sub_f32_e32 v9, v6, v16
	v_fmamk_f32 v10, v8, 0x3e9b6dac, v148
	v_sub_f32_e32 v9, v5, v9
	v_mul_f32_e32 v5, v6, v8
	v_fmaak_f32 v115, v8, v10, 0x3f2aaada
	v_ldexp_f32 v11, v9, 1
	v_pk_mul_f32 v[8:9], v[4:5], v[114:115]
	v_ldexp_f32 v7, v6, 1
	v_fma_f32 v6, v4, s27, -v8
	v_fmac_f32_e32 v6, 0xb102e308, v4
	v_pk_add_f32 v[4:5], v[8:9], v[6:7]
	v_mov_b32_e32 v10, v8
	v_sub_f32_e32 v14, v5, v7
	v_pk_add_f32 v[12:13], v[4:5], v[8:9] neg_lo:[0,1] neg_hi:[0,1]
	v_sub_f32_e32 v8, v9, v14
	v_add_f32_e32 v11, v11, v8
	v_pk_add_f32 v[8:9], v[4:5], v[10:11]
	v_mov_b32_e32 v7, v4
	v_mov_b32_e32 v13, v9
	v_pk_add_f32 v[16:17], v[6:7], v[12:13] neg_lo:[0,1] neg_hi:[0,1]
	v_pk_add_f32 v[6:7], v[6:7], v[12:13]
	v_mov_b32_e32 v15, v4
	v_pk_add_f32 v[12:13], v[6:7], v[4:5] op_sel:[1,0] op_sel_hi:[0,1] neg_lo:[0,1] neg_hi:[0,1]
	v_mov_b32_e32 v14, v11
	v_mov_b32_e32 v10, v9
	v_mov_b32_e32 v11, v7
	v_pk_mov_b32 v[4:5], v[4:5], v[12:13] op_sel:[1,0]
	v_pk_add_f32 v[8:9], v[8:9], v[12:13] op_sel_hi:[1,0] neg_lo:[0,1] neg_hi:[0,1]
	v_pk_add_f32 v[4:5], v[10:11], v[4:5] neg_lo:[0,1] neg_hi:[0,1]
	v_mov_b32_e32 v8, v16
	v_pk_add_f32 v[4:5], v[14:15], v[4:5] neg_lo:[0,1] neg_hi:[0,1]
	v_mov_b32_e32 v17, v7
	v_pk_add_f32 v[8:9], v[8:9], v[4:5]
	s_nop 0
	v_pk_add_f32 v[10:11], v[8:9], v[8:9] op_sel:[0,1] op_sel_hi:[1,0]
	s_nop 0
	v_pk_add_f32 v[6:7], v[6:7], v[10:11] op_sel:[1,0] op_sel_hi:[0,1]
	v_mov_b32_e32 v9, v6
	v_mov_b32_e32 v5, v10
	v_pk_add_f32 v[10:11], v[8:9], v[16:17] neg_lo:[0,1] neg_hi:[0,1]
	s_nop 0
	v_sub_f32_e32 v7, v8, v10
	v_pk_add_f32 v[4:5], v[4:5], v[10:11] neg_lo:[0,1] neg_hi:[0,1]
	v_sub_f32_e32 v7, v16, v7
	v_add_f32_e32 v4, v4, v7
	v_add_f32_e32 v4, v4, v5
	v_add_f32_e32 v4, v6, v4
	v_cndmask_b32_e32 v4, v149, v4, vcc
	v_cmp_ngt_f32_e32 vcc, -1.0, v18
	s_nop 1
	v_cndmask_b32_e32 v4, v150, v4, vcc
	v_cmp_neq_f32_e32 vcc, -1.0, v18
	s_nop 1
	v_cndmask_b32_e32 v4, v151, v4, vcc
	v_cmp_lt_f32_e64 vcc, |v18|, s40
	s_nop 1
	v_cndmask_b32_e32 v4, v4, v18, vcc
	v_add_f32_e32 v0, v0, v4
	v_xor_b32_e32 v6, 0x80000000, v0
; DI float sigmoidf_(float x) { return __builtin_amdgcn_rcpf(1.f + __expf(-x)); }
; DI float softplusf_(float x) { return fmaxf(x, 0.f) + log1pf(__expf(-fabsf(x))); }
; DI void phase_xnorm(const Params& p, int bid, int nb, char* lds) {
;     ...
;       for (int r = 0; r < 4; ++r) { const float xx = acc[r]; float res;
;         if (j < 8) res = -softplusf_(-(xx + p.b_fgate[j]));
;         else if (j < 12) res = sigmoidf_(xx);
;         else res = -__expf(p.a_log[j - 12]) * softplusf_(xx + p.dt_bias[j - 12]);
;         small[(size_t)(row0 + r) * 16 + j] = res; }
.LBB0_103:
	s_or_b64 exec, exec, s[34:35]
	v_lshl_add_u64 v[4:5], s[84:85], 0, v[102:103]
	v_add_co_u32_e32 v8, vcc, 0x1700000, v4
	s_nop 1
	v_addc_co_u32_e32 v9, vcc, 0, v5, vcc
	global_store_dword v[8:9], v6, off
	s_and_saveexec_b64 s[34:35], s[6:7]
	s_xor_b64 s[34:35], exec, s[34:35]
	s_cbranch_execz .LBB0_109
	s_and_saveexec_b64 s[38:39], s[8:9]
	s_xor_b64 s[38:39], exec, s[38:39]
	s_cbranch_execz .LBB0_106
	v_mov_b32_e32 v0, v240
	v_mov_b32_e32 v6, v241
	v_add_f32_e32 v0, v1, v0
	v_mul_f32_e64 v7, |v0|, s18
	v_exp_f32_e32 v20, v7
	v_mul_f32_e32 v6, 0x3fb8aa3b, v6
	v_exp_f32_e32 v21, v6
	v_max_f32_e32 v0, 0, v0
	v_add_f32_e32 v8, 1.0, v20
	v_add_f32_e32 v9, -1.0, v8
	v_frexp_mant_f32_e32 v10, v8
	v_cvt_f64_f32_e32 v[6:7], v8
	v_sub_f32_e32 v11, v9, v8
	v_frexp_exp_i32_f64_e32 v6, v[6:7]
	v_cmp_gt_f32_e32 vcc, s19, v10
	v_sub_f32_e32 v9, v20, v9
	v_add_f32_e32 v7, 1.0, v11
	v_subbrev_co_u32_e32 v6, vcc, 0, v6, vcc
	v_add_f32_e32 v7, v9, v7
	v_sub_u32_e32 v9, 0, v6
	v_ldexp_f32 v8, v8, v9
	v_add_f32_e32 v10, -1.0, v8
	v_add_f32_e32 v11, 1.0, v8
	v_ldexp_f32 v7, v7, v9
	v_add_f32_e32 v9, 1.0, v10
	v_add_f32_e32 v12, -1.0, v11
	v_sub_f32_e32 v9, v8, v9
	v_sub_f32_e32 v8, v8, v12
	v_add_f32_e32 v12, v7, v9
	v_add_f32_e32 v7, v7, v8
	v_add_f32_e32 v14, v11, v7
	v_rcp_f32_e32 v15, v14
	v_add_f32_e32 v9, v10, v12
	v_sub_f32_e32 v10, v9, v10
	v_sub_f32_e32 v8, v14, v11
	v_mul_f32_e32 v17, v9, v15
	v_sub_f32_e32 v16, v12, v10
	v_mul_f32_e32 v10, v14, v17
	v_sub_f32_e32 v7, v7, v8
	v_fma_f32 v12, v17, v14, -v10
	v_fmac_f32_e32 v12, v17, v7
	v_add_f32_e32 v8, v10, v12
	v_sub_f32_e32 v11, v9, v8
	v_mov_b32_e32 v13, v8
	v_pk_add_f32 v[8:9], v[8:9], v[10:11] neg_lo:[0,1] neg_hi:[0,1]
	v_cvt_f32_i32_e32 v6, v6
	v_pk_add_f32 v[8:9], v[8:9], v[12:13] neg_lo:[0,1] neg_hi:[0,1]
	v_cmp_neq_f32_e32 vcc, s29, v20
	v_add_f32_e32 v9, v16, v9
	v_add_f32_e32 v8, v8, v9
	v_add_f32_e32 v9, v11, v8
	v_mul_f32_e32 v13, v15, v9
	v_mul_f32_e32 v10, v14, v13
	v_sub_f32_e32 v11, v11, v9
	v_add_f32_e32 v18, v17, v13
	v_fma_f32 v12, v13, v14, -v10
	v_add_f32_e32 v16, v8, v11
	v_sub_f32_e32 v8, v18, v17
	v_fmac_f32_e32 v12, v13, v7
	v_sub_f32_e32 v7, v13, v8
	v_add_f32_e32 v8, v10, v12
	v_sub_f32_e32 v11, v9, v8
	v_mov_b32_e32 v13, v8
	v_pk_add_f32 v[8:9], v[8:9], v[10:11] neg_lo:[0,1] neg_hi:[0,1]
	s_nop 0
	v_pk_add_f32 v[8:9], v[8:9], v[12:13] neg_lo:[0,1] neg_hi:[0,1]
	s_nop 0
	v_add_f32_e32 v9, v16, v9
	v_add_f32_e32 v8, v8, v9
	v_add_f32_e32 v8, v11, v8
	v_mul_f32_e32 v8, v15, v8
	v_add_f32_e32 v7, v7, v8
	v_add_f32_e32 v8, v18, v7
	v_mul_f32_e32 v10, v8, v8
	v_sub_f32_e32 v11, v8, v18
	v_fmamk_f32 v12, v10, 0x3e9b6dac, v148
	v_sub_f32_e32 v11, v7, v11
	v_mul_f32_e32 v7, v8, v10
	v_fmaak_f32 v115, v10, v12, 0x3f2aaada
	v_ldexp_f32 v13, v11, 1
	v_pk_mul_f32 v[10:11], v[6:7], v[114:115]
	v_ldexp_f32 v9, v8, 1
	v_fma_f32 v8, v6, s27, -v10
	v_fmac_f32_e32 v8, 0xb102e308, v6
	v_pk_add_f32 v[6:7], v[10:11], v[8:9]
	v_mov_b32_e32 v12, v10
	v_sub_f32_e32 v16, v7, v9
	v_pk_add_f32 v[14:15], v[6:7], v[10:11] neg_lo:[0,1] neg_hi:[0,1]
	v_sub_f32_e32 v10, v11, v16
	v_add_f32_e32 v13, v13, v10
	v_pk_add_f32 v[10:11], v[6:7], v[12:13]
	v_mov_b32_e32 v9, v6
	v_mov_b32_e32 v15, v11
	v_pk_add_f32 v[18:19], v[8:9], v[14:15] neg_lo:[0,1] neg_hi:[0,1]
	v_pk_add_f32 v[8:9], v[8:9], v[14:15]
	v_mov_b32_e32 v17, v6
	v_pk_add_f32 v[14:15], v[8:9], v[6:7] op_sel:[1,0] op_sel_hi:[0,1] neg_lo:[0,1] neg_hi:[0,1]
	v_mov_b32_e32 v16, v13
	v_mov_b32_e32 v12, v11
	v_mov_b32_e32 v13, v9
	v_pk_mov_b32 v[6:7], v[6:7], v[14:15] op_sel:[1,0]
	v_pk_add_f32 v[10:11], v[10:11], v[14:15] op_sel_hi:[1,0] neg_lo:[0,1] neg_hi:[0,1]
	v_pk_add_f32 v[6:7], v[12:13], v[6:7] neg_lo:[0,1] neg_hi:[0,1]
	v_mov_b32_e32 v10, v18
	v_pk_add_f32 v[6:7], v[16:17], v[6:7] neg_lo:[0,1] neg_hi:[0,1]
	v_mov_b32_e32 v19, v9
	v_pk_add_f32 v[10:11], v[10:11], v[6:7]
	s_nop 0
	v_pk_add_f32 v[12:13], v[10:11], v[10:11] op_sel:[0,1] op_sel_hi:[1,0]
	s_nop 0
	v_pk_add_f32 v[8:9], v[8:9], v[12:13] op_sel:[1,0] op_sel_hi:[0,1]
	v_mov_b32_e32 v11, v8
	v_mov_b32_e32 v7, v12
	v_pk_add_f32 v[12:13], v[10:11], v[18:19] neg_lo:[0,1] neg_hi:[0,1]
	s_nop 0
	v_sub_f32_e32 v9, v10, v12
	v_pk_add_f32 v[6:7], v[6:7], v[12:13] neg_lo:[0,1] neg_hi:[0,1]
	v_sub_f32_e32 v9, v18, v9
	v_add_f32_e32 v6, v6, v9
	v_add_f32_e32 v6, v6, v7
	v_add_f32_e32 v6, v8, v6
	v_cndmask_b32_e32 v6, v149, v6, vcc
	v_cmp_ngt_f32_e32 vcc, -1.0, v20
	s_nop 1
	v_cndmask_b32_e32 v6, v150, v6, vcc
	v_cmp_neq_f32_e32 vcc, -1.0, v20
	s_nop 1
	v_cndmask_b32_e32 v6, v151, v6, vcc
	v_cmp_lt_f32_e64 vcc, |v20|, s40
	s_nop 1
	v_cndmask_b32_e32 v6, v6, v20, vcc
	v_add_f32_e32 v0, v0, v6
	v_mul_f32_e64 v0, v0, -v21

; DI float softplusf_(float x) { return fmaxf(x, 0.f) + log1pf(__expf(-fabsf(x))); }
; DI void phase_xnorm(const Params& p, int bid, int nb, char* lds) {
;     ...
;       for (int r = 0; r < 4; ++r) { const float xx = acc[r]; float res;
;         if (j < 8) res = -softplusf_(-(xx + p.b_fgate[j]));
.LBB0_109:
	s_andn2_saveexec_b64 s[34:35], s[34:35]
	s_cbranch_execz .LBB0_111
	v_mov_b32_e32 v0, v242
	v_add_f32_e32 v0, v1, v0
	v_mul_f32_e64 v1, |v0|, s18
	v_exp_f32_e32 v18, v1
	v_max_f32_e64 v19, -v0, 0
	v_add_f32_e32 v6, 1.0, v18
	v_add_f32_e32 v7, -1.0, v6
	v_frexp_mant_f32_e32 v8, v6
	v_cvt_f64_f32_e32 v[0:1], v6
	v_sub_f32_e32 v9, v7, v6
	v_frexp_exp_i32_f64_e32 v0, v[0:1]
	v_cmp_gt_f32_e32 vcc, s19, v8
	v_sub_f32_e32 v7, v18, v7
	v_add_f32_e32 v1, 1.0, v9
	v_subbrev_co_u32_e32 v0, vcc, 0, v0, vcc
	v_add_f32_e32 v1, v7, v1
	v_sub_u32_e32 v7, 0, v0
	v_ldexp_f32 v6, v6, v7
	v_add_f32_e32 v8, -1.0, v6
	v_add_f32_e32 v9, 1.0, v6
	v_ldexp_f32 v1, v1, v7
	v_add_f32_e32 v7, 1.0, v8
	v_add_f32_e32 v10, -1.0, v9
	v_sub_f32_e32 v7, v6, v7
	v_sub_f32_e32 v6, v6, v10
	v_add_f32_e32 v10, v1, v7
	v_add_f32_e32 v1, v1, v6
	v_add_f32_e32 v12, v9, v1
	v_rcp_f32_e32 v13, v12
	v_add_f32_e32 v7, v8, v10
	v_sub_f32_e32 v8, v7, v8
	v_sub_f32_e32 v6, v12, v9
	v_mul_f32_e32 v15, v7, v13
	v_sub_f32_e32 v14, v10, v8
	v_mul_f32_e32 v8, v12, v15
	v_sub_f32_e32 v1, v1, v6
	v_fma_f32 v10, v15, v12, -v8
	v_fmac_f32_e32 v10, v15, v1
	v_add_f32_e32 v6, v8, v10
	v_sub_f32_e32 v9, v7, v6
	v_mov_b32_e32 v11, v6
	v_pk_add_f32 v[6:7], v[6:7], v[8:9] neg_lo:[0,1] neg_hi:[0,1]
	v_cvt_f32_i32_e32 v0, v0
	v_pk_add_f32 v[6:7], v[6:7], v[10:11] neg_lo:[0,1] neg_hi:[0,1]
	v_cmp_neq_f32_e32 vcc, s29, v18
	v_add_f32_e32 v7, v14, v7
	v_add_f32_e32 v6, v6, v7
	v_add_f32_e32 v7, v9, v6
	v_mul_f32_e32 v11, v13, v7
	v_mul_f32_e32 v8, v12, v11
	v_sub_f32_e32 v9, v9, v7
	v_add_f32_e32 v16, v15, v11
	v_fma_f32 v10, v11, v12, -v8
	v_add_f32_e32 v14, v6, v9
	v_sub_f32_e32 v6, v16, v15
	v_fmac_f32_e32 v10, v11, v1
	v_sub_f32_e32 v1, v11, v6
	v_add_f32_e32 v6, v8, v10
	v_sub_f32_e32 v9, v7, v6
	v_mov_b32_e32 v11, v6
	v_pk_add_f32 v[6:7], v[6:7], v[8:9] neg_lo:[0,1] neg_hi:[0,1]
	s_nop 0
	v_pk_add_f32 v[6:7], v[6:7], v[10:11] neg_lo:[0,1] neg_hi:[0,1]
	s_nop 0
	v_add_f32_e32 v7, v14, v7
	v_add_f32_e32 v6, v6, v7
	v_add_f32_e32 v6, v9, v6
	v_mul_f32_e32 v6, v13, v6
	v_add_f32_e32 v1, v1, v6
	v_add_f32_e32 v6, v16, v1
	v_mul_f32_e32 v8, v6, v6
	v_sub_f32_e32 v9, v6, v16
	v_fmamk_f32 v10, v8, 0x3e9b6dac, v148
	v_sub_f32_e32 v9, v1, v9
	v_mul_f32_e32 v1, v6, v8
	v_fmaak_f32 v115, v8, v10, 0x3f2aaada
	v_ldexp_f32 v11, v9, 1
	v_pk_mul_f32 v[8:9], v[0:1], v[114:115]
	v_ldexp_f32 v7, v6, 1
	v_fma_f32 v6, v0, s27, -v8
	v_fmac_f32_e32 v6, 0xb102e308, v0
	v_pk_add_f32 v[0:1], v[8:9], v[6:7]
	v_mov_b32_e32 v10, v8
	v_sub_f32_e32 v14, v1, v7
	v_pk_add_f32 v[12:13], v[0:1], v[8:9] neg_lo:[0,1] neg_hi:[0,1]
	v_sub_f32_e32 v8, v9, v14
	v_add_f32_e32 v11, v11, v8
	v_pk_add_f32 v[8:9], v[0:1], v[10:11]
	v_mov_b32_e32 v7, v0
	v_mov_b32_e32 v13, v9
	v_pk_add_f32 v[16:17], v[6:7], v[12:13] neg_lo:[0,1] neg_hi:[0,1]
	v_pk_add_f32 v[6:7], v[6:7], v[12:13]
	v_mov_b32_e32 v15, v0
	v_pk_add_f32 v[12:13], v[6:7], v[0:1] op_sel:[1,0] op_sel_hi:[0,1] neg_lo:[0,1] neg_hi:[0,1]
	v_mov_b32_e32 v14, v11
	v_mov_b32_e32 v10, v9
	v_mov_b32_e32 v11, v7
	v_pk_mov_b32 v[0:1], v[0:1], v[12:13] op_sel:[1,0]
	v_pk_add_f32 v[8:9], v[8:9], v[12:13] op_sel_hi:[1,0] neg_lo:[0,1] neg_hi:[0,1]
	v_pk_add_f32 v[0:1], v[10:11], v[0:1] neg_lo:[0,1] neg_hi:[0,1]
	v_mov_b32_e32 v8, v16
	v_pk_add_f32 v[0:1], v[14:15], v[0:1] neg_lo:[0,1] neg_hi:[0,1]
	v_mov_b32_e32 v17, v7
	v_pk_add_f32 v[8:9], v[8:9], v[0:1]
	s_nop 0
	v_pk_add_f32 v[10:11], v[8:9], v[8:9] op_sel:[0,1] op_sel_hi:[1,0]
	s_nop 0
	v_pk_add_f32 v[6:7], v[6:7], v[10:11] op_sel:[1,0] op_sel_hi:[0,1]
	v_mov_b32_e32 v9, v6
	v_mov_b32_e32 v1, v10
	v_pk_add_f32 v[10:11], v[8:9], v[16:17] neg_lo:[0,1] neg_hi:[0,1]
	s_nop 0
	v_sub_f32_e32 v7, v8, v10
	v_pk_add_f32 v[0:1], v[0:1], v[10:11] neg_lo:[0,1] neg_hi:[0,1]
	v_sub_f32_e32 v7, v16, v7
	v_add_f32_e32 v0, v0, v7
	v_add_f32_e32 v0, v0, v1
	v_add_f32_e32 v0, v6, v0
	v_cndmask_b32_e32 v0, v149, v0, vcc
	v_cmp_ngt_f32_e32 vcc, -1.0, v18
	s_nop 1
	v_cndmask_b32_e32 v0, v150, v0, vcc
	v_cmp_neq_f32_e32 vcc, -1.0, v18
	s_nop 1
	v_cndmask_b32_e32 v0, v151, v0, vcc
	v_cmp_lt_f32_e64 vcc, |v18|, s40
	s_nop 1
	v_cndmask_b32_e32 v0, v0, v18, vcc
	v_add_f32_e32 v0, v19, v0
	v_xor_b32_e32 v0, 0x80000000, v0
; DI float sigmoidf_(float x) { return __builtin_amdgcn_rcpf(1.f + __expf(-x)); }
; DI float softplusf_(float x) { return fmaxf(x, 0.f) + log1pf(__expf(-fabsf(x))); }
; DI void phase_xnorm(const Params& p, int bid, int nb, char* lds) {
;     ...
;       for (int r = 0; r < 4; ++r) { const float xx = acc[r]; float res;
;         if (j < 8) res = -softplusf_(-(xx + p.b_fgate[j]));
;         else if (j < 12) res = sigmoidf_(xx);
;         else res = -__expf(p.a_log[j - 12]) * softplusf_(xx + p.dt_bias[j - 12]);
;         small[(size_t)(row0 + r) * 16 + j] = res; }
.LBB0_111:
	s_or_b64 exec, exec, s[34:35]
	v_add_co_u32_e32 v6, vcc, 0x1700000, v4
	s_nop 1
	v_addc_co_u32_e32 v7, vcc, 0, v5, vcc
	global_store_dword v[6:7], v0, off offset:64
	s_and_saveexec_b64 s[34:35], s[6:7]
	s_xor_b64 s[34:35], exec, s[34:35]
	s_cbranch_execz .LBB0_117
	s_and_saveexec_b64 s[38:39], s[8:9]
	s_xor_b64 s[38:39], exec, s[38:39]
	s_cbranch_execz .LBB0_114
	v_mov_b32_e32 v0, v240
	v_mov_b32_e32 v1, v241
	v_add_f32_e32 v0, v2, v0
	v_mul_f32_e64 v6, |v0|, s18
	v_exp_f32_e32 v18, v6
	v_mul_f32_e32 v1, 0x3fb8aa3b, v1
	v_exp_f32_e32 v19, v1
	v_max_f32_e32 v20, 0, v0
	v_add_f32_e32 v6, 1.0, v18
	v_add_f32_e32 v7, -1.0, v6
	v_frexp_mant_f32_e32 v8, v6
	v_cvt_f64_f32_e32 v[0:1], v6
	v_sub_f32_e32 v9, v7, v6
	v_frexp_exp_i32_f64_e32 v0, v[0:1]
	v_cmp_gt_f32_e32 vcc, s19, v8
	v_sub_f32_e32 v7, v18, v7
	v_add_f32_e32 v1, 1.0, v9
	v_subbrev_co_u32_e32 v0, vcc, 0, v0, vcc
	v_add_f32_e32 v1, v7, v1
	v_sub_u32_e32 v7, 0, v0
	v_ldexp_f32 v6, v6, v7
	v_add_f32_e32 v8, -1.0, v6
	v_add_f32_e32 v9, 1.0, v6
	v_ldexp_f32 v1, v1, v7
	v_add_f32_e32 v7, 1.0, v8
	v_add_f32_e32 v10, -1.0, v9
	v_sub_f32_e32 v7, v6, v7
	v_sub_f32_e32 v6, v6, v10
	v_add_f32_e32 v10, v1, v7
	v_add_f32_e32 v1, v1, v6
	v_add_f32_e32 v12, v9, v1
	v_rcp_f32_e32 v13, v12
	v_add_f32_e32 v7, v8, v10
	v_sub_f32_e32 v8, v7, v8
	v_sub_f32_e32 v6, v12, v9
	v_mul_f32_e32 v15, v7, v13
	v_sub_f32_e32 v14, v10, v8
	v_mul_f32_e32 v8, v12, v15
	v_sub_f32_e32 v1, v1, v6
	v_fma_f32 v10, v15, v12, -v8
	v_fmac_f32_e32 v10, v15, v1
	v_add_f32_e32 v6, v8, v10
	v_sub_f32_e32 v9, v7, v6
	v_mov_b32_e32 v11, v6
	v_pk_add_f32 v[6:7], v[6:7], v[8:9] neg_lo:[0,1] neg_hi:[0,1]
	v_cvt_f32_i32_e32 v0, v0
	v_pk_add_f32 v[6:7], v[6:7], v[10:11] neg_lo:[0,1] neg_hi:[0,1]
	v_cmp_neq_f32_e32 vcc, s29, v18
	v_add_f32_e32 v7, v14, v7
	v_add_f32_e32 v6, v6, v7
	v_add_f32_e32 v7, v9, v6
	v_mul_f32_e32 v11, v13, v7
	v_mul_f32_e32 v8, v12, v11
	v_sub_f32_e32 v9, v9, v7
	v_add_f32_e32 v16, v15, v11
	v_fma_f32 v10, v11, v12, -v8
	v_add_f32_e32 v14, v6, v9
	v_sub_f32_e32 v6, v16, v15
	v_fmac_f32_e32 v10, v11, v1
	v_sub_f32_e32 v1, v11, v6
	v_add_f32_e32 v6, v8, v10
	v_sub_f32_e32 v9, v7, v6
	v_mov_b32_e32 v11, v6
	v_pk_add_f32 v[6:7], v[6:7], v[8:9] neg_lo:[0,1] neg_hi:[0,1]
	s_nop 0
	v_pk_add_f32 v[6:7], v[6:7], v[10:11] neg_lo:[0,1] neg_hi:[0,1]
	s_nop 0
	v_add_f32_e32 v7, v14, v7
	v_add_f32_e32 v6, v6, v7
	v_add_f32_e32 v6, v9, v6
	v_mul_f32_e32 v6, v13, v6
	v_add_f32_e32 v1, v1, v6
	v_add_f32_e32 v6, v16, v1
	v_mul_f32_e32 v8, v6, v6
	v_sub_f32_e32 v9, v6, v16
	v_fmamk_f32 v10, v8, 0x3e9b6dac, v148
	v_sub_f32_e32 v9, v1, v9
	v_mul_f32_e32 v1, v6, v8
	v_fmaak_f32 v115, v8, v10, 0x3f2aaada
	v_ldexp_f32 v11, v9, 1
	v_pk_mul_f32 v[8:9], v[0:1], v[114:115]
	v_ldexp_f32 v7, v6, 1
	v_fma_f32 v6, v0, s27, -v8
	v_fmac_f32_e32 v6, 0xb102e308, v0
	v_pk_add_f32 v[0:1], v[8:9], v[6:7]
	v_mov_b32_e32 v10, v8
	v_sub_f32_e32 v14, v1, v7
	v_pk_add_f32 v[12:13], v[0:1], v[8:9] neg_lo:[0,1] neg_hi:[0,1]
	v_sub_f32_e32 v8, v9, v14
	v_add_f32_e32 v11, v11, v8
	v_pk_add_f32 v[8:9], v[0:1], v[10:11]
	v_mov_b32_e32 v7, v0
	v_mov_b32_e32 v13, v9
	v_pk_add_f32 v[16:17], v[6:7], v[12:13] neg_lo:[0,1] neg_hi:[0,1]
	v_pk_add_f32 v[6:7], v[6:7], v[12:13]
	v_mov_b32_e32 v15, v0
	v_pk_add_f32 v[12:13], v[6:7], v[0:1] op_sel:[1,0] op_sel_hi:[0,1] neg_lo:[0,1] neg_hi:[0,1]
	v_mov_b32_e32 v14, v11
	v_mov_b32_e32 v10, v9
	v_mov_b32_e32 v11, v7
	v_pk_mov_b32 v[0:1], v[0:1], v[12:13] op_sel:[1,0]
	v_pk_add_f32 v[8:9], v[8:9], v[12:13] op_sel_hi:[1,0] neg_lo:[0,1] neg_hi:[0,1]
	v_pk_add_f32 v[0:1], v[10:11], v[0:1] neg_lo:[0,1] neg_hi:[0,1]
	v_mov_b32_e32 v8, v16
	v_pk_add_f32 v[0:1], v[14:15], v[0:1] neg_lo:[0,1] neg_hi:[0,1]
	v_mov_b32_e32 v17, v7
	v_pk_add_f32 v[8:9], v[8:9], v[0:1]
	s_nop 0
	v_pk_add_f32 v[10:11], v[8:9], v[8:9] op_sel:[0,1] op_sel_hi:[1,0]
	s_nop 0
	v_pk_add_f32 v[6:7], v[6:7], v[10:11] op_sel:[1,0] op_sel_hi:[0,1]
	v_mov_b32_e32 v9, v6
	v_mov_b32_e32 v1, v10
	v_pk_add_f32 v[10:11], v[8:9], v[16:17] neg_lo:[0,1] neg_hi:[0,1]
	s_nop 0
	v_sub_f32_e32 v7, v8, v10
	v_pk_add_f32 v[0:1], v[0:1], v[10:11] neg_lo:[0,1] neg_hi:[0,1]
	v_sub_f32_e32 v7, v16, v7
	v_add_f32_e32 v0, v0, v7
	v_add_f32_e32 v0, v0, v1
	v_add_f32_e32 v0, v6, v0
	v_cndmask_b32_e32 v0, v149, v0, vcc
	v_cmp_ngt_f32_e32 vcc, -1.0, v18
	s_nop 1
	v_cndmask_b32_e32 v0, v150, v0, vcc
	v_cmp_neq_f32_e32 vcc, -1.0, v18
	s_nop 1
	v_cndmask_b32_e32 v0, v151, v0, vcc
	v_cmp_lt_f32_e64 vcc, |v18|, s40
	s_nop 1
	v_cndmask_b32_e32 v0, v0, v18, vcc
	v_add_f32_e32 v0, v20, v0
	v_mul_f32_e64 v0, v0, -v19

; DI float softplusf_(float x) { return fmaxf(x, 0.f) + log1pf(__expf(-fabsf(x))); }
; DI void phase_xnorm(const Params& p, int bid, int nb, char* lds) {
;     ...
;       for (int r = 0; r < 4; ++r) { const float xx = acc[r]; float res;
;         if (j < 8) res = -softplusf_(-(xx + p.b_fgate[j]));
.LBB0_117:
	s_andn2_saveexec_b64 s[34:35], s[34:35]
	s_cbranch_execz .LBB0_119
	v_mov_b32_e32 v0, v242
	v_add_f32_e32 v0, v2, v0
	v_mul_f32_e64 v1, |v0|, s18
	v_exp_f32_e32 v2, v1
	v_max_f32_e64 v18, -v0, 0
	v_add_f32_e32 v6, 1.0, v2
	v_add_f32_e32 v7, -1.0, v6
	v_frexp_mant_f32_e32 v8, v6
	v_cvt_f64_f32_e32 v[0:1], v6
	v_sub_f32_e32 v9, v7, v6
	v_frexp_exp_i32_f64_e32 v0, v[0:1]
	v_cmp_gt_f32_e32 vcc, s19, v8
	v_sub_f32_e32 v7, v2, v7
	v_add_f32_e32 v1, 1.0, v9
	v_subbrev_co_u32_e32 v0, vcc, 0, v0, vcc
	v_add_f32_e32 v1, v7, v1
	v_sub_u32_e32 v7, 0, v0
	v_ldexp_f32 v6, v6, v7
	v_add_f32_e32 v8, -1.0, v6
	v_add_f32_e32 v9, 1.0, v6
	v_ldexp_f32 v1, v1, v7
	v_add_f32_e32 v7, 1.0, v8
	v_add_f32_e32 v10, -1.0, v9
	v_sub_f32_e32 v7, v6, v7
	v_sub_f32_e32 v6, v6, v10
	v_add_f32_e32 v10, v1, v7
	v_add_f32_e32 v1, v1, v6
	v_add_f32_e32 v12, v9, v1
	v_rcp_f32_e32 v13, v12
	v_add_f32_e32 v7, v8, v10
	v_sub_f32_e32 v8, v7, v8
	v_sub_f32_e32 v6, v12, v9
	v_mul_f32_e32 v15, v7, v13
	v_sub_f32_e32 v14, v10, v8
	v_mul_f32_e32 v8, v12, v15
	v_sub_f32_e32 v1, v1, v6
	v_fma_f32 v10, v15, v12, -v8
	v_fmac_f32_e32 v10, v15, v1
	v_add_f32_e32 v6, v8, v10
	v_sub_f32_e32 v9, v7, v6
	v_mov_b32_e32 v11, v6
	v_pk_add_f32 v[6:7], v[6:7], v[8:9] neg_lo:[0,1] neg_hi:[0,1]
	v_cvt_f32_i32_e32 v0, v0
	v_pk_add_f32 v[6:7], v[6:7], v[10:11] neg_lo:[0,1] neg_hi:[0,1]
	v_cmp_neq_f32_e32 vcc, s29, v2
	v_add_f32_e32 v7, v14, v7
	v_add_f32_e32 v6, v6, v7
	v_add_f32_e32 v7, v9, v6
	v_mul_f32_e32 v11, v13, v7
	v_mul_f32_e32 v8, v12, v11
	v_sub_f32_e32 v9, v9, v7
	v_add_f32_e32 v16, v15, v11
	v_fma_f32 v10, v11, v12, -v8
	v_add_f32_e32 v14, v6, v9
	v_sub_f32_e32 v6, v16, v15
	v_fmac_f32_e32 v10, v11, v1
	v_sub_f32_e32 v1, v11, v6
	v_add_f32_e32 v6, v8, v10
	v_sub_f32_e32 v9, v7, v6
	v_mov_b32_e32 v11, v6
	v_pk_add_f32 v[6:7], v[6:7], v[8:9] neg_lo:[0,1] neg_hi:[0,1]
	s_nop 0
	v_pk_add_f32 v[6:7], v[6:7], v[10:11] neg_lo:[0,1] neg_hi:[0,1]
	s_nop 0
	v_add_f32_e32 v7, v14, v7
	v_add_f32_e32 v6, v6, v7
	v_add_f32_e32 v6, v9, v6
	v_mul_f32_e32 v6, v13, v6
	v_add_f32_e32 v1, v1, v6
	v_add_f32_e32 v6, v16, v1
	v_mul_f32_e32 v8, v6, v6
	v_sub_f32_e32 v9, v6, v16
	v_fmamk_f32 v10, v8, 0x3e9b6dac, v148
	v_sub_f32_e32 v9, v1, v9
	v_mul_f32_e32 v1, v6, v8
	v_fmaak_f32 v115, v8, v10, 0x3f2aaada
	v_ldexp_f32 v11, v9, 1
	v_pk_mul_f32 v[8:9], v[0:1], v[114:115]
	v_ldexp_f32 v7, v6, 1
	v_fma_f32 v6, v0, s27, -v8
	v_fmac_f32_e32 v6, 0xb102e308, v0
	v_pk_add_f32 v[0:1], v[8:9], v[6:7]
	v_mov_b32_e32 v10, v8
	v_sub_f32_e32 v14, v1, v7
	v_pk_add_f32 v[12:13], v[0:1], v[8:9] neg_lo:[0,1] neg_hi:[0,1]
	v_sub_f32_e32 v8, v9, v14
	v_add_f32_e32 v11, v11, v8
	v_pk_add_f32 v[8:9], v[0:1], v[10:11]
	v_mov_b32_e32 v7, v0
	v_mov_b32_e32 v13, v9
	v_pk_add_f32 v[16:17], v[6:7], v[12:13] neg_lo:[0,1] neg_hi:[0,1]
	v_pk_add_f32 v[6:7], v[6:7], v[12:13]
	v_mov_b32_e32 v15, v0
	v_pk_add_f32 v[12:13], v[6:7], v[0:1] op_sel:[1,0] op_sel_hi:[0,1] neg_lo:[0,1] neg_hi:[0,1]
	v_mov_b32_e32 v14, v11
	v_mov_b32_e32 v10, v9
	v_mov_b32_e32 v11, v7
	v_pk_mov_b32 v[0:1], v[0:1], v[12:13] op_sel:[1,0]
	v_pk_add_f32 v[8:9], v[8:9], v[12:13] op_sel_hi:[1,0] neg_lo:[0,1] neg_hi:[0,1]
	v_pk_add_f32 v[0:1], v[10:11], v[0:1] neg_lo:[0,1] neg_hi:[0,1]
	v_mov_b32_e32 v8, v16
	v_pk_add_f32 v[0:1], v[14:15], v[0:1] neg_lo:[0,1] neg_hi:[0,1]
	v_mov_b32_e32 v17, v7
	v_pk_add_f32 v[8:9], v[8:9], v[0:1]
	s_nop 0
	v_pk_add_f32 v[10:11], v[8:9], v[8:9] op_sel:[0,1] op_sel_hi:[1,0]
	s_nop 0
	v_pk_add_f32 v[6:7], v[6:7], v[10:11] op_sel:[1,0] op_sel_hi:[0,1]
	v_mov_b32_e32 v9, v6
	v_mov_b32_e32 v1, v10
	v_pk_add_f32 v[10:11], v[8:9], v[16:17] neg_lo:[0,1] neg_hi:[0,1]
	s_nop 0
	v_sub_f32_e32 v7, v8, v10
	v_pk_add_f32 v[0:1], v[0:1], v[10:11] neg_lo:[0,1] neg_hi:[0,1]
	v_sub_f32_e32 v7, v16, v7
	v_add_f32_e32 v0, v0, v7
	v_add_f32_e32 v0, v0, v1
	v_add_f32_e32 v0, v6, v0
	v_cndmask_b32_e32 v0, v149, v0, vcc
	v_cmp_ngt_f32_e32 vcc, -1.0, v2
	s_nop 1
	v_cndmask_b32_e32 v0, v150, v0, vcc
	v_cmp_neq_f32_e32 vcc, -1.0, v2
	s_nop 1
	v_cndmask_b32_e32 v0, v151, v0, vcc
	v_cmp_lt_f32_e64 vcc, |v2|, s40
	s_nop 1
	v_cndmask_b32_e32 v0, v0, v2, vcc
	v_add_f32_e32 v0, v18, v0
	v_xor_b32_e32 v0, 0x80000000, v0
; DI float sigmoidf_(float x) { return __builtin_amdgcn_rcpf(1.f + __expf(-x)); }
; DI float softplusf_(float x) { return fmaxf(x, 0.f) + log1pf(__expf(-fabsf(x))); }
; DI void phase_xnorm(const Params& p, int bid, int nb, char* lds) {
;     ...
;       for (int r = 0; r < 4; ++r) { const float xx = acc[r]; float res;
;         if (j < 8) res = -softplusf_(-(xx + p.b_fgate[j]));
;         else if (j < 12) res = sigmoidf_(xx);
;         else res = -__expf(p.a_log[j - 12]) * softplusf_(xx + p.dt_bias[j - 12]);
;         small[(size_t)(row0 + r) * 16 + j] = res; }
.LBB0_119:
	s_or_b64 exec, exec, s[34:35]
	v_add_co_u32_e32 v6, vcc, 0x1700000, v4
	s_nop 1
	v_addc_co_u32_e32 v7, vcc, 0, v5, vcc
	global_store_dword v[6:7], v0, off offset:128
	s_and_saveexec_b64 s[34:35], s[6:7]
	s_xor_b64 s[34:35], exec, s[34:35]
	s_cbranch_execz .LBB0_125
	s_and_saveexec_b64 s[38:39], s[8:9]
	s_xor_b64 s[38:39], exec, s[38:39]
	s_cbranch_execz .LBB0_122
	v_mov_b32_e32 v0, v240
	v_mov_b32_e32 v1, v241
	v_add_f32_e32 v0, v3, v0
	v_mul_f32_e64 v2, |v0|, s18
	v_exp_f32_e32 v16, v2
	v_mul_f32_e32 v1, 0x3fb8aa3b, v1
	v_exp_f32_e32 v17, v1
	v_max_f32_e32 v18, 0, v0
	v_add_f32_e32 v2, 1.0, v16
	v_add_f32_e32 v3, -1.0, v2
	v_frexp_mant_f32_e32 v6, v2
	v_cvt_f64_f32_e32 v[0:1], v2
	v_sub_f32_e32 v7, v3, v2
	v_frexp_exp_i32_f64_e32 v0, v[0:1]
	v_cmp_gt_f32_e32 vcc, s19, v6
	v_sub_f32_e32 v3, v16, v3
	v_add_f32_e32 v1, 1.0, v7
	v_subbrev_co_u32_e32 v0, vcc, 0, v0, vcc
	v_add_f32_e32 v1, v3, v1
	v_sub_u32_e32 v3, 0, v0
	v_ldexp_f32 v2, v2, v3
	v_add_f32_e32 v6, -1.0, v2
	v_add_f32_e32 v7, 1.0, v2
	v_ldexp_f32 v1, v1, v3
	v_add_f32_e32 v3, 1.0, v6
	v_add_f32_e32 v8, -1.0, v7
	v_sub_f32_e32 v3, v2, v3
	v_sub_f32_e32 v2, v2, v8
	v_add_f32_e32 v8, v1, v3
	v_add_f32_e32 v1, v1, v2
	v_add_f32_e32 v10, v7, v1
	v_rcp_f32_e32 v11, v10
	v_add_f32_e32 v3, v6, v8
	v_sub_f32_e32 v6, v3, v6
	v_sub_f32_e32 v2, v10, v7
	v_mul_f32_e32 v13, v3, v11
	v_sub_f32_e32 v12, v8, v6
	v_mul_f32_e32 v6, v10, v13
	v_sub_f32_e32 v1, v1, v2
	v_fma_f32 v8, v13, v10, -v6
	v_fmac_f32_e32 v8, v13, v1
	v_add_f32_e32 v2, v6, v8
	v_sub_f32_e32 v7, v3, v2
	v_mov_b32_e32 v9, v2
	v_pk_add_f32 v[2:3], v[2:3], v[6:7] neg_lo:[0,1] neg_hi:[0,1]
	v_cvt_f32_i32_e32 v0, v0
	v_pk_add_f32 v[2:3], v[2:3], v[8:9] neg_lo:[0,1] neg_hi:[0,1]
	v_cmp_neq_f32_e32 vcc, s29, v16
	v_add_f32_e32 v3, v12, v3
	v_add_f32_e32 v2, v2, v3
	v_add_f32_e32 v3, v7, v2
	v_mul_f32_e32 v9, v11, v3
	v_mul_f32_e32 v6, v10, v9
	v_sub_f32_e32 v7, v7, v3
	v_add_f32_e32 v14, v13, v9
	v_fma_f32 v8, v9, v10, -v6
	v_add_f32_e32 v12, v2, v7
	v_sub_f32_e32 v2, v14, v13
	v_fmac_f32_e32 v8, v9, v1
	v_sub_f32_e32 v1, v9, v2
	v_add_f32_e32 v2, v6, v8
	v_sub_f32_e32 v7, v3, v2
	v_mov_b32_e32 v9, v2
	v_pk_add_f32 v[2:3], v[2:3], v[6:7] neg_lo:[0,1] neg_hi:[0,1]
	s_nop 0
	v_pk_add_f32 v[2:3], v[2:3], v[8:9] neg_lo:[0,1] neg_hi:[0,1]
	s_nop 0
	v_add_f32_e32 v3, v12, v3
	v_add_f32_e32 v2, v2, v3
	v_add_f32_e32 v2, v7, v2
	v_mul_f32_e32 v2, v11, v2
	v_add_f32_e32 v1, v1, v2
	v_add_f32_e32 v2, v14, v1
	v_mul_f32_e32 v6, v2, v2
	v_sub_f32_e32 v7, v2, v14
	v_fmamk_f32 v8, v6, 0x3e9b6dac, v148
	v_sub_f32_e32 v7, v1, v7
	v_mul_f32_e32 v1, v2, v6
	v_fmaak_f32 v115, v6, v8, 0x3f2aaada
	v_ldexp_f32 v9, v7, 1
	v_pk_mul_f32 v[6:7], v[0:1], v[114:115]
	v_ldexp_f32 v3, v2, 1
	v_fma_f32 v2, v0, s27, -v6
	v_fmac_f32_e32 v2, 0xb102e308, v0
	v_pk_add_f32 v[0:1], v[6:7], v[2:3]
	v_mov_b32_e32 v8, v6
	v_sub_f32_e32 v12, v1, v3
	v_pk_add_f32 v[10:11], v[0:1], v[6:7] neg_lo:[0,1] neg_hi:[0,1]
	v_sub_f32_e32 v6, v7, v12
	v_add_f32_e32 v9, v9, v6
	v_pk_add_f32 v[6:7], v[0:1], v[8:9]
	v_mov_b32_e32 v3, v0
	v_mov_b32_e32 v11, v7
	v_pk_add_f32 v[14:15], v[2:3], v[10:11] neg_lo:[0,1] neg_hi:[0,1]
	v_pk_add_f32 v[2:3], v[2:3], v[10:11]
	v_mov_b32_e32 v13, v0
	v_pk_add_f32 v[10:11], v[2:3], v[0:1] op_sel:[1,0] op_sel_hi:[0,1] neg_lo:[0,1] neg_hi:[0,1]
	v_mov_b32_e32 v12, v9
	v_mov_b32_e32 v8, v7
	v_mov_b32_e32 v9, v3
	v_pk_mov_b32 v[0:1], v[0:1], v[10:11] op_sel:[1,0]
	v_pk_add_f32 v[6:7], v[6:7], v[10:11] op_sel_hi:[1,0] neg_lo:[0,1] neg_hi:[0,1]
	v_pk_add_f32 v[0:1], v[8:9], v[0:1] neg_lo:[0,1] neg_hi:[0,1]
	v_mov_b32_e32 v6, v14
	v_pk_add_f32 v[0:1], v[12:13], v[0:1] neg_lo:[0,1] neg_hi:[0,1]
	v_mov_b32_e32 v15, v3
	v_pk_add_f32 v[6:7], v[6:7], v[0:1]
	s_nop 0
	v_pk_add_f32 v[8:9], v[6:7], v[6:7] op_sel:[0,1] op_sel_hi:[1,0]
	s_nop 0
	v_pk_add_f32 v[2:3], v[2:3], v[8:9] op_sel:[1,0] op_sel_hi:[0,1]
	v_mov_b32_e32 v7, v2
	v_mov_b32_e32 v1, v8
	v_pk_add_f32 v[8:9], v[6:7], v[14:15] neg_lo:[0,1] neg_hi:[0,1]
	s_nop 0
	v_sub_f32_e32 v3, v6, v8
	v_pk_add_f32 v[0:1], v[0:1], v[8:9] neg_lo:[0,1] neg_hi:[0,1]
	v_sub_f32_e32 v3, v14, v3
	v_add_f32_e32 v0, v0, v3
	v_add_f32_e32 v0, v0, v1
	v_add_f32_e32 v0, v2, v0
	v_cndmask_b32_e32 v0, v149, v0, vcc
	v_cmp_ngt_f32_e32 vcc, -1.0, v16
	s_nop 1
	v_cndmask_b32_e32 v0, v150, v0, vcc
	v_cmp_neq_f32_e32 vcc, -1.0, v16
	s_nop 1
	v_cndmask_b32_e32 v0, v151, v0, vcc
	v_cmp_lt_f32_e64 vcc, |v16|, s40
	s_nop 1
	v_cndmask_b32_e32 v0, v0, v16, vcc
	v_add_f32_e32 v0, v18, v0
	v_mul_f32_e64 v6, v0, -v17

; DI float softplusf_(float x) { return fmaxf(x, 0.f) + log1pf(__expf(-fabsf(x))); }
; DI void phase_xnorm(const Params& p, int bid, int nb, char* lds) {
;     ...
;       for (int r = 0; r < 4; ++r) { const float xx = acc[r]; float res;
;         if (j < 8) res = -softplusf_(-(xx + p.b_fgate[j]));
.LBB0_125:
	s_andn2_saveexec_b64 s[34:35], s[34:35]
	s_cbranch_execz .LBB0_92
	v_mov_b32_e32 v0, v242
	v_add_f32_e32 v0, v3, v0
	v_mul_f32_e64 v1, |v0|, s18
	v_exp_f32_e32 v16, v1
	v_max_f32_e64 v17, -v0, 0
	v_add_f32_e32 v2, 1.0, v16
	v_add_f32_e32 v3, -1.0, v2
	v_frexp_mant_f32_e32 v6, v2
	v_cvt_f64_f32_e32 v[0:1], v2
	v_sub_f32_e32 v7, v3, v2
	v_frexp_exp_i32_f64_e32 v0, v[0:1]
	v_cmp_gt_f32_e32 vcc, s19, v6
	v_sub_f32_e32 v3, v16, v3
	v_add_f32_e32 v1, 1.0, v7
	v_subbrev_co_u32_e32 v0, vcc, 0, v0, vcc
	v_add_f32_e32 v1, v3, v1
	v_sub_u32_e32 v3, 0, v0
	v_ldexp_f32 v2, v2, v3
	v_add_f32_e32 v6, -1.0, v2
	v_add_f32_e32 v7, 1.0, v2
	v_ldexp_f32 v1, v1, v3
	v_add_f32_e32 v3, 1.0, v6
	v_add_f32_e32 v8, -1.0, v7
	v_sub_f32_e32 v3, v2, v3
	v_sub_f32_e32 v2, v2, v8
	v_add_f32_e32 v8, v1, v3
	v_add_f32_e32 v1, v1, v2
	v_add_f32_e32 v10, v7, v1
	v_rcp_f32_e32 v11, v10
	v_add_f32_e32 v3, v6, v8
	v_sub_f32_e32 v6, v3, v6
	v_sub_f32_e32 v2, v10, v7
	v_mul_f32_e32 v13, v3, v11
	v_sub_f32_e32 v12, v8, v6
	v_mul_f32_e32 v6, v10, v13
	v_sub_f32_e32 v1, v1, v2
	v_fma_f32 v8, v13, v10, -v6
	v_fmac_f32_e32 v8, v13, v1
	v_add_f32_e32 v2, v6, v8
	v_sub_f32_e32 v7, v3, v2
	v_mov_b32_e32 v9, v2
	v_pk_add_f32 v[2:3], v[2:3], v[6:7] neg_lo:[0,1] neg_hi:[0,1]
	v_cvt_f32_i32_e32 v0, v0
	v_pk_add_f32 v[2:3], v[2:3], v[8:9] neg_lo:[0,1] neg_hi:[0,1]
	v_cmp_neq_f32_e32 vcc, s29, v16
	v_add_f32_e32 v3, v12, v3
	v_add_f32_e32 v2, v2, v3
	v_add_f32_e32 v3, v7, v2
	v_mul_f32_e32 v9, v11, v3
	v_mul_f32_e32 v6, v10, v9
	v_sub_f32_e32 v7, v7, v3
	v_add_f32_e32 v14, v13, v9
	v_fma_f32 v8, v9, v10, -v6
	v_add_f32_e32 v12, v2, v7
	v_sub_f32_e32 v2, v14, v13
	v_fmac_f32_e32 v8, v9, v1
	v_sub_f32_e32 v1, v9, v2
	v_add_f32_e32 v2, v6, v8
	v_sub_f32_e32 v7, v3, v2
	v_mov_b32_e32 v9, v2
	v_pk_add_f32 v[2:3], v[2:3], v[6:7] neg_lo:[0,1] neg_hi:[0,1]
	s_nop 0
	v_pk_add_f32 v[2:3], v[2:3], v[8:9] neg_lo:[0,1] neg_hi:[0,1]
	s_nop 0
	v_add_f32_e32 v3, v12, v3
	v_add_f32_e32 v2, v2, v3
	v_add_f32_e32 v2, v7, v2
	v_mul_f32_e32 v2, v11, v2
	v_add_f32_e32 v1, v1, v2
	v_add_f32_e32 v2, v14, v1
	v_mul_f32_e32 v6, v2, v2
	v_sub_f32_e32 v7, v2, v14
	v_fmamk_f32 v8, v6, 0x3e9b6dac, v148
	v_sub_f32_e32 v7, v1, v7
	v_mul_f32_e32 v1, v2, v6
	v_fmaak_f32 v115, v6, v8, 0x3f2aaada
	v_ldexp_f32 v9, v7, 1
	v_pk_mul_f32 v[6:7], v[0:1], v[114:115]
	v_ldexp_f32 v3, v2, 1
	v_fma_f32 v2, v0, s27, -v6
	v_fmac_f32_e32 v2, 0xb102e308, v0
	v_pk_add_f32 v[0:1], v[6:7], v[2:3]
	v_mov_b32_e32 v8, v6
	v_sub_f32_e32 v12, v1, v3
	v_pk_add_f32 v[10:11], v[0:1], v[6:7] neg_lo:[0,1] neg_hi:[0,1]
	v_sub_f32_e32 v6, v7, v12
	v_add_f32_e32 v9, v9, v6
	v_pk_add_f32 v[6:7], v[0:1], v[8:9]
	v_mov_b32_e32 v3, v0
	v_mov_b32_e32 v11, v7
	v_pk_add_f32 v[14:15], v[2:3], v[10:11] neg_lo:[0,1] neg_hi:[0,1]
	v_pk_add_f32 v[2:3], v[2:3], v[10:11]
	v_mov_b32_e32 v13, v0
	v_pk_add_f32 v[10:11], v[2:3], v[0:1] op_sel:[1,0] op_sel_hi:[0,1] neg_lo:[0,1] neg_hi:[0,1]
	v_mov_b32_e32 v12, v9
	v_mov_b32_e32 v8, v7
	v_mov_b32_e32 v9, v3
	v_pk_mov_b32 v[0:1], v[0:1], v[10:11] op_sel:[1,0]
	v_pk_add_f32 v[6:7], v[6:7], v[10:11] op_sel_hi:[1,0] neg_lo:[0,1] neg_hi:[0,1]
	v_pk_add_f32 v[0:1], v[8:9], v[0:1] neg_lo:[0,1] neg_hi:[0,1]
	v_mov_b32_e32 v6, v14
	v_pk_add_f32 v[0:1], v[12:13], v[0:1] neg_lo:[0,1] neg_hi:[0,1]
	v_mov_b32_e32 v15, v3
	v_pk_add_f32 v[6:7], v[6:7], v[0:1]
	s_nop 0
	v_pk_add_f32 v[8:9], v[6:7], v[6:7] op_sel:[0,1] op_sel_hi:[1,0]
	s_nop 0
	v_pk_add_f32 v[2:3], v[2:3], v[8:9] op_sel:[1,0] op_sel_hi:[0,1]
	v_mov_b32_e32 v7, v2
	v_mov_b32_e32 v1, v8
	v_pk_add_f32 v[8:9], v[6:7], v[14:15] neg_lo:[0,1] neg_hi:[0,1]
	s_nop 0
	v_sub_f32_e32 v3, v6, v8
	v_pk_add_f32 v[0:1], v[0:1], v[8:9] neg_lo:[0,1] neg_hi:[0,1]
	v_sub_f32_e32 v3, v14, v3
	v_add_f32_e32 v0, v0, v3
	v_add_f32_e32 v0, v0, v1
	v_add_f32_e32 v0, v2, v0
	v_cndmask_b32_e32 v0, v149, v0, vcc
	v_cmp_ngt_f32_e32 vcc, -1.0, v16
	s_nop 1
	v_cndmask_b32_e32 v0, v150, v0, vcc
	v_cmp_neq_f32_e32 vcc, -1.0, v16
	s_nop 1
	v_cndmask_b32_e32 v0, v151, v0, vcc
	v_cmp_lt_f32_e64 vcc, |v16|, s40
	s_nop 1
	v_cndmask_b32_e32 v0, v0, v16, vcc
	v_add_f32_e32 v0, v17, v0
	v_xor_b32_e32 v6, 0x80000000, v0
	s_branch .LBB0_92
